# v024 + redundant post-barrier lgkmcnt(0) waits deleted in the GEMM loops (one issue slot per MFMA block)
# baseline (speedup 1.0000x reference)
.LBB0_261:
	ds_read_b128 v[144:147], v170
	ds_read_b128 v[148:151], v170 offset:1024
	ds_read_b128 v[174:177], v170 offset:2048
	ds_read_b128 v[178:181], v170 offset:3072
	ds_read_b128 v[182:185], v171
	ds_read_b128 v[186:189], v171 offset:1024
	ds_read_b128 v[190:193], v171 offset:2048
	ds_read_b128 v[194:197], v171 offset:3072
	s_add_u32 s26, s80, 0xfff80080
	s_addc_u32 s27, s81, -1
	s_cmp_eq_u32 vcc_hi, 28
	s_cselect_b32 s83, s69, s27
	s_cselect_b32 s82, s75, s26
	s_cselect_b32 s27, s57, vcc_lo
	s_cselect_b32 s26, s96, s97
	v_lshl_add_u64 v[152:153], s[80:81], 0, v[134:135]
	s_add_i32 m0, s87, 0xc000
	ds_read_b128 v[198:201], v172
	ds_read_b128 v[202:205], v172 offset:1024
	ds_read_b128 v[206:209], v172 offset:2048
	ds_read_b128 v[210:213], v172 offset:3072
	ds_read_b128 v[214:217], v172 offset:4096
	ds_read_b128 v[220:223], v172 offset:5120
	ds_read_b128 v[224:227], v172 offset:6144
	ds_read_b128 v[228:231], v172 offset:7168
	global_load_lds_dwordx4 v[152:153], off
	v_lshl_add_u64 v[152:153], s[80:81], 0, v[138:139]
	s_add_i32 m0, s87, 0xe000
	s_nop 0
	global_load_lds_dwordx4 v[152:153], off
	s_waitcnt vmcnt(8)
	s_waitcnt lgkmcnt(0)
	s_barrier
	v_mfma_f32_16x16x32_bf16 v[122:125], v[144:147], v[198:201], v[122:125]
	v_mfma_f32_16x16x32_bf16 v[118:121], v[174:177], v[198:201], v[118:121]
	v_mfma_f32_16x16x32_bf16 v[106:109], v[144:147], v[206:209], v[106:109]
	v_mfma_f32_16x16x32_bf16 v[102:105], v[174:177], v[206:209], v[102:105]
	v_mfma_f32_16x16x32_bf16 v[90:93], v[144:147], v[214:217], v[90:93]
	v_mfma_f32_16x16x32_bf16 v[86:89], v[174:177], v[214:217], v[86:89]
	v_mfma_f32_16x16x32_bf16 v[74:77], v[144:147], v[224:227], v[74:77]
	v_mfma_f32_16x16x32_bf16 v[70:73], v[174:177], v[224:227], v[70:73]
	v_mfma_f32_16x16x32_bf16 v[122:125], v[148:151], v[202:205], v[122:125]
	v_mfma_f32_16x16x32_bf16 v[118:121], v[178:181], v[202:205], v[118:121]
	v_mfma_f32_16x16x32_bf16 v[106:109], v[148:151], v[210:213], v[106:109]
	v_mfma_f32_16x16x32_bf16 v[102:105], v[178:181], v[210:213], v[102:105]
	v_mfma_f32_16x16x32_bf16 v[90:93], v[148:151], v[220:223], v[90:93]
	v_mfma_f32_16x16x32_bf16 v[86:89], v[178:181], v[220:223], v[86:89]
	v_mfma_f32_16x16x32_bf16 v[74:77], v[148:151], v[228:231], v[74:77]
	v_mfma_f32_16x16x32_bf16 v[70:73], v[178:181], v[228:231], v[70:73]
	v_mfma_f32_16x16x32_bf16 v[126:129], v[182:185], v[198:201], v[126:129]
	v_mfma_f32_16x16x32_bf16 v[114:117], v[190:193], v[198:201], v[114:117]
	v_mfma_f32_16x16x32_bf16 v[110:113], v[182:185], v[206:209], v[110:113]
	v_mfma_f32_16x16x32_bf16 v[98:101], v[190:193], v[206:209], v[98:101]
	v_mfma_f32_16x16x32_bf16 v[94:97], v[182:185], v[214:217], v[94:97]
	v_mfma_f32_16x16x32_bf16 v[82:85], v[190:193], v[214:217], v[82:85]
	v_mfma_f32_16x16x32_bf16 v[78:81], v[182:185], v[224:227], v[78:81]
	v_mfma_f32_16x16x32_bf16 v[66:69], v[190:193], v[224:227], v[66:69]
	v_mfma_f32_16x16x32_bf16 v[126:129], v[186:189], v[202:205], v[126:129]
	v_mfma_f32_16x16x32_bf16 v[114:117], v[194:197], v[202:205], v[114:117]
	v_mfma_f32_16x16x32_bf16 v[110:113], v[186:189], v[210:213], v[110:113]
	v_mfma_f32_16x16x32_bf16 v[98:101], v[194:197], v[210:213], v[98:101]
	v_mfma_f32_16x16x32_bf16 v[94:97], v[186:189], v[220:223], v[94:97]
	v_mfma_f32_16x16x32_bf16 v[82:85], v[194:197], v[220:223], v[82:85]
	v_mfma_f32_16x16x32_bf16 v[78:81], v[186:189], v[228:231], v[78:81]
	v_mfma_f32_16x16x32_bf16 v[66:69], v[194:197], v[228:231], v[66:69]
	s_barrier
	v_lshl_add_u64 v[152:153], s[26:27], 0, v[162:163]
	s_add_i32 s26, s94, s86
	s_mov_b32 m0, s26
	ds_read_b128 v[198:201], v172 offset:16384
	ds_read_b128 v[202:205], v172 offset:17408
	ds_read_b128 v[206:209], v172 offset:18432
	ds_read_b128 v[210:213], v172 offset:19456
	ds_read_b128 v[214:217], v172 offset:20480
	ds_read_b128 v[220:223], v172 offset:21504
	ds_read_b128 v[224:227], v172 offset:22528
	ds_read_b128 v[228:231], v172 offset:23552
	global_load_lds_dwordx4 v[152:153], off
	v_lshl_add_u64 v[232:233], v[152:153], 0, s[10:11]
	s_add_i32 m0, s26, 0x2000
	s_add_i32 s26, s95, s86
	global_load_lds_dwordx4 v[232:233], off
	v_lshl_add_u64 v[232:233], v[152:153], 0, s[12:13]
	s_mov_b32 m0, s26
	v_lshl_add_u64 v[234:235], s[82:83], 0, v[132:133]
	global_load_lds_dwordx4 v[232:233], off
	v_lshl_add_u64 v[232:233], v[152:153], 0, s[14:15]
	s_add_i32 m0, s26, 0x2000
	s_nop 0
	global_load_lds_dwordx4 v[232:233], off
	v_lshl_add_u64 v[232:233], s[82:83], 0, v[130:131]
	s_mov_b32 m0, s87
	s_nop 0
	global_load_lds_dwordx4 v[232:233], off
	s_mov_b32 m0, s88
	s_nop 0
	global_load_lds_dwordx4 v[234:235], off
	s_waitcnt vmcnt(8)
	s_waitcnt lgkmcnt(0)
	s_barrier
	v_mfma_f32_16x16x32_bf16 v[58:61], v[144:147], v[198:201], v[58:61]
	v_mfma_f32_16x16x32_bf16 v[54:57], v[174:177], v[198:201], v[54:57]
	v_mfma_f32_16x16x32_bf16 v[42:45], v[144:147], v[206:209], v[42:45]
	v_mfma_f32_16x16x32_bf16 v[38:41], v[174:177], v[206:209], v[38:41]
	v_mfma_f32_16x16x32_bf16 v[26:29], v[144:147], v[214:217], v[26:29]
	v_mfma_f32_16x16x32_bf16 v[22:25], v[174:177], v[214:217], v[22:25]
	v_mfma_f32_16x16x32_bf16 v[10:13], v[144:147], v[224:227], v[10:13]
	v_mfma_f32_16x16x32_bf16 v[6:9], v[174:177], v[224:227], v[6:9]
	v_mfma_f32_16x16x32_bf16 v[58:61], v[148:151], v[202:205], v[58:61]
	v_mfma_f32_16x16x32_bf16 v[54:57], v[178:181], v[202:205], v[54:57]
	v_mfma_f32_16x16x32_bf16 v[42:45], v[148:151], v[210:213], v[42:45]
	v_mfma_f32_16x16x32_bf16 v[38:41], v[178:181], v[210:213], v[38:41]
	v_mfma_f32_16x16x32_bf16 v[26:29], v[148:151], v[220:223], v[26:29]
	v_mfma_f32_16x16x32_bf16 v[22:25], v[178:181], v[220:223], v[22:25]
	v_mfma_f32_16x16x32_bf16 v[10:13], v[148:151], v[228:231], v[10:13]
	v_mfma_f32_16x16x32_bf16 v[6:9], v[178:181], v[228:231], v[6:9]
	v_mfma_f32_16x16x32_bf16 v[62:65], v[182:185], v[198:201], v[62:65]
	v_mfma_f32_16x16x32_bf16 v[50:53], v[190:193], v[198:201], v[50:53]
	v_mfma_f32_16x16x32_bf16 v[46:49], v[182:185], v[206:209], v[46:49]
	v_mfma_f32_16x16x32_bf16 v[34:37], v[190:193], v[206:209], v[34:37]
	v_mfma_f32_16x16x32_bf16 v[30:33], v[182:185], v[214:217], v[30:33]
	v_mfma_f32_16x16x32_bf16 v[18:21], v[190:193], v[214:217], v[18:21]
	v_mfma_f32_16x16x32_bf16 v[14:17], v[182:185], v[224:227], v[14:17]
	v_mfma_f32_16x16x32_bf16 v[2:5], v[190:193], v[224:227], v[2:5]
	v_mfma_f32_16x16x32_bf16 v[62:65], v[186:189], v[202:205], v[62:65]
	v_mfma_f32_16x16x32_bf16 v[50:53], v[194:197], v[202:205], v[50:53]
	v_mfma_f32_16x16x32_bf16 v[46:49], v[186:189], v[210:213], v[46:49]
	v_mfma_f32_16x16x32_bf16 v[34:37], v[194:197], v[210:213], v[34:37]
	v_mfma_f32_16x16x32_bf16 v[30:33], v[186:189], v[220:223], v[30:33]
	v_mfma_f32_16x16x32_bf16 v[18:21], v[194:197], v[220:223], v[18:21]
	v_mfma_f32_16x16x32_bf16 v[14:17], v[186:189], v[228:231], v[14:17]
	v_mfma_f32_16x16x32_bf16 v[2:5], v[194:197], v[228:231], v[2:5]
	s_barrier
	s_add_i32 s33, 0, 0x18000
	v_add_u32_e32 v136, s33, v167
	s_add_i32 s8, 0, 0x1c000
	ds_read_b128 v[144:147], v136
	ds_read_b128 v[148:151], v136 offset:1024
	ds_read_b128 v[174:177], v136 offset:2048
	ds_read_b128 v[178:181], v136 offset:3072
	v_add_u32_e32 v136, s8, v167
	ds_read_b128 v[182:185], v136
	ds_read_b128 v[186:189], v136 offset:1024
	ds_read_b128 v[190:193], v136 offset:2048
	ds_read_b128 v[194:197], v136 offset:3072
	s_add_u32 s26, s82, 0x80000
	s_addc_u32 s27, s83, 0
	s_mov_b32 m0, s89
	v_lshl_add_u64 v[236:237], s[26:27], 0, v[130:131]
	ds_read_b128 v[198:201], v172 offset:32768
	ds_read_b128 v[202:205], v172 offset:33792
	ds_read_b128 v[206:209], v172 offset:34816
	ds_read_b128 v[210:213], v172 offset:35840
	ds_read_b128 v[214:217], v172 offset:36864
	ds_read_b128 v[220:223], v172 offset:37888
	ds_read_b128 v[224:227], v172 offset:38912
	ds_read_b128 v[228:231], v172 offset:39936
	global_load_lds_dwordx4 v[236:237], off
	v_lshl_add_u64 v[236:237], s[26:27], 0, v[132:133]
	s_mov_b32 m0, s90
	s_nop 0
	global_load_lds_dwordx4 v[236:237], off
	s_waitcnt vmcnt(8)
	s_waitcnt lgkmcnt(0)
	s_barrier
	v_mfma_f32_16x16x32_bf16 v[122:125], v[144:147], v[198:201], v[122:125]
	v_mfma_f32_16x16x32_bf16 v[118:121], v[174:177], v[198:201], v[118:121]
	v_mfma_f32_16x16x32_bf16 v[106:109], v[144:147], v[206:209], v[106:109]
	v_mfma_f32_16x16x32_bf16 v[102:105], v[174:177], v[206:209], v[102:105]
	v_mfma_f32_16x16x32_bf16 v[90:93], v[144:147], v[214:217], v[90:93]
	v_mfma_f32_16x16x32_bf16 v[86:89], v[174:177], v[214:217], v[86:89]
	v_mfma_f32_16x16x32_bf16 v[74:77], v[144:147], v[224:227], v[74:77]
	v_mfma_f32_16x16x32_bf16 v[70:73], v[174:177], v[224:227], v[70:73]
	v_mfma_f32_16x16x32_bf16 v[122:125], v[148:151], v[202:205], v[122:125]
	v_mfma_f32_16x16x32_bf16 v[118:121], v[178:181], v[202:205], v[118:121]
	v_mfma_f32_16x16x32_bf16 v[106:109], v[148:151], v[210:213], v[106:109]
	v_mfma_f32_16x16x32_bf16 v[102:105], v[178:181], v[210:213], v[102:105]
	v_mfma_f32_16x16x32_bf16 v[90:93], v[148:151], v[220:223], v[90:93]
	v_mfma_f32_16x16x32_bf16 v[86:89], v[178:181], v[220:223], v[86:89]
	v_mfma_f32_16x16x32_bf16 v[74:77], v[148:151], v[228:231], v[74:77]
	v_mfma_f32_16x16x32_bf16 v[70:73], v[178:181], v[228:231], v[70:73]
	v_mfma_f32_16x16x32_bf16 v[126:129], v[182:185], v[198:201], v[126:129]
	v_mfma_f32_16x16x32_bf16 v[114:117], v[190:193], v[198:201], v[114:117]
	v_mfma_f32_16x16x32_bf16 v[110:113], v[182:185], v[206:209], v[110:113]
	v_mfma_f32_16x16x32_bf16 v[98:101], v[190:193], v[206:209], v[98:101]
	v_mfma_f32_16x16x32_bf16 v[94:97], v[182:185], v[214:217], v[94:97]
	v_mfma_f32_16x16x32_bf16 v[82:85], v[190:193], v[214:217], v[82:85]
	v_mfma_f32_16x16x32_bf16 v[78:81], v[182:185], v[224:227], v[78:81]
	v_mfma_f32_16x16x32_bf16 v[66:69], v[190:193], v[224:227], v[66:69]
	v_mfma_f32_16x16x32_bf16 v[126:129], v[186:189], v[202:205], v[126:129]
	v_mfma_f32_16x16x32_bf16 v[114:117], v[194:197], v[202:205], v[114:117]
	v_mfma_f32_16x16x32_bf16 v[110:113], v[186:189], v[210:213], v[110:113]
	v_mfma_f32_16x16x32_bf16 v[98:101], v[194:197], v[210:213], v[98:101]
	v_mfma_f32_16x16x32_bf16 v[94:97], v[186:189], v[220:223], v[94:97]
	v_mfma_f32_16x16x32_bf16 v[82:85], v[194:197], v[220:223], v[82:85]
	v_mfma_f32_16x16x32_bf16 v[78:81], v[186:189], v[228:231], v[78:81]
	v_mfma_f32_16x16x32_bf16 v[66:69], v[194:197], v[228:231], v[66:69]
	s_barrier
	s_add_i32 s9, s33, s86
	v_lshl_add_u64 v[236:237], v[152:153], 0, s[20:21]
	s_mov_b32 m0, s9
	ds_read_b128 v[198:201], v172 offset:49152
	ds_read_b128 v[202:205], v172 offset:50176
	ds_read_b128 v[206:209], v172 offset:51200
	ds_read_b128 v[210:213], v172 offset:52224
	ds_read_b128 v[214:217], v172 offset:53248
	ds_read_b128 v[220:223], v172 offset:54272
	ds_read_b128 v[224:227], v172 offset:55296
	ds_read_b128 v[228:231], v172 offset:56320
	global_load_lds_dwordx4 v[236:237], off
	v_lshl_add_u64 v[236:237], v[152:153], 0, s[22:23]
	s_add_i32 m0, s9, 0x2000
	s_add_i32 s8, s8, s86
	global_load_lds_dwordx4 v[236:237], off
	v_lshl_add_u64 v[236:237], v[152:153], 0, s[40:41]
	s_mov_b32 m0, s8
	v_lshl_add_u64 v[152:153], v[152:153], 0, s[44:45]
	global_load_lds_dwordx4 v[236:237], off
	s_add_i32 m0, s8, 0x2000
	s_nop 0
	global_load_lds_dwordx4 v[152:153], off
	v_lshl_add_u64 v[152:153], v[232:233], 0, s[24:25]
	s_mov_b32 m0, s91
	s_nop 0
	global_load_lds_dwordx4 v[152:153], off
	v_lshl_add_u64 v[152:153], v[234:235], 0, s[24:25]
	s_mov_b32 m0, s92
	s_nop 0
	global_load_lds_dwordx4 v[152:153], off
	s_waitcnt vmcnt(8)
	s_waitcnt lgkmcnt(0)
	s_barrier
	v_mfma_f32_16x16x32_bf16 v[58:61], v[144:147], v[198:201], v[58:61]
	v_mfma_f32_16x16x32_bf16 v[54:57], v[174:177], v[198:201], v[54:57]
	v_mfma_f32_16x16x32_bf16 v[42:45], v[144:147], v[206:209], v[42:45]
	v_mfma_f32_16x16x32_bf16 v[38:41], v[174:177], v[206:209], v[38:41]
	v_mfma_f32_16x16x32_bf16 v[26:29], v[144:147], v[214:217], v[26:29]
	v_mfma_f32_16x16x32_bf16 v[22:25], v[174:177], v[214:217], v[22:25]
	v_mfma_f32_16x16x32_bf16 v[10:13], v[144:147], v[224:227], v[10:13]
	v_mfma_f32_16x16x32_bf16 v[6:9], v[174:177], v[224:227], v[6:9]
	v_mfma_f32_16x16x32_bf16 v[58:61], v[148:151], v[202:205], v[58:61]
	v_mfma_f32_16x16x32_bf16 v[54:57], v[178:181], v[202:205], v[54:57]
	v_mfma_f32_16x16x32_bf16 v[42:45], v[148:151], v[210:213], v[42:45]
	v_mfma_f32_16x16x32_bf16 v[38:41], v[178:181], v[210:213], v[38:41]
	v_mfma_f32_16x16x32_bf16 v[26:29], v[148:151], v[220:223], v[26:29]
	v_mfma_f32_16x16x32_bf16 v[22:25], v[178:181], v[220:223], v[22:25]
	v_mfma_f32_16x16x32_bf16 v[10:13], v[148:151], v[228:231], v[10:13]
	v_mfma_f32_16x16x32_bf16 v[6:9], v[178:181], v[228:231], v[6:9]
	v_mfma_f32_16x16x32_bf16 v[62:65], v[182:185], v[198:201], v[62:65]
	v_mfma_f32_16x16x32_bf16 v[50:53], v[190:193], v[198:201], v[50:53]
	v_mfma_f32_16x16x32_bf16 v[46:49], v[182:185], v[206:209], v[46:49]
	v_mfma_f32_16x16x32_bf16 v[34:37], v[190:193], v[206:209], v[34:37]
	v_mfma_f32_16x16x32_bf16 v[30:33], v[182:185], v[214:217], v[30:33]
	v_mfma_f32_16x16x32_bf16 v[18:21], v[190:193], v[214:217], v[18:21]
	v_mfma_f32_16x16x32_bf16 v[14:17], v[182:185], v[224:227], v[14:17]
	v_mfma_f32_16x16x32_bf16 v[2:5], v[190:193], v[224:227], v[2:5]
	v_mfma_f32_16x16x32_bf16 v[62:65], v[186:189], v[202:205], v[62:65]
	v_mfma_f32_16x16x32_bf16 v[50:53], v[194:197], v[202:205], v[50:53]
	v_mfma_f32_16x16x32_bf16 v[46:49], v[186:189], v[210:213], v[46:49]
	v_mfma_f32_16x16x32_bf16 v[34:37], v[194:197], v[210:213], v[34:37]
	v_mfma_f32_16x16x32_bf16 v[30:33], v[186:189], v[220:223], v[30:33]
	v_mfma_f32_16x16x32_bf16 v[18:21], v[194:197], v[220:223], v[18:21]
	v_mfma_f32_16x16x32_bf16 v[14:17], v[186:189], v[228:231], v[14:17]
	v_mfma_f32_16x16x32_bf16 v[2:5], v[194:197], v[228:231], v[2:5]
	s_barrier
	s_add_i32 vcc_hi, vcc_hi, 2
	s_add_u32 s97, s97, 0x10000
	s_addc_u32 vcc_lo, vcc_lo, 0
	s_add_u32 s80, s80, 0x100
	s_addc_u32 s81, s81, 0
	s_cmp_gt_u32 vcc_hi, 29
	s_cbranch_scc0 .LBB0_261
	s_and_b64 vcc, exec, s[50:51]
	s_cbranch_vccz .LBB0_264
	s_barrier

.LBB0_285:
	ds_read_b128 v[26:29], v1
	ds_read_b128 v[30:33], v1 offset:1024
	ds_read_b128 v[18:21], v1 offset:2048
	ds_read_b128 v[22:25], v1 offset:3072
	ds_read_b128 v[10:13], v185
	ds_read_b128 v[14:17], v185 offset:1024
	ds_read_b128 v[2:5], v185 offset:2048
	ds_read_b128 v[6:9], v185 offset:3072
	s_add_u32 s26, s70, 0xfffc0080
	s_addc_u32 s27, s71, -1
	s_cmp_eq_u32 s94, 12
	s_cselect_b32 s73, s51, s27
	s_cselect_b32 s72, s90, s26
	s_cselect_b32 s75, s45, s93
	s_cselect_b32 s74, s91, s92
	v_lshl_add_u64 v[176:177], s[70:71], 0, v[168:169]
	s_add_i32 m0, s33, 0xc000
	ds_read_b128 v[190:193], v186
	ds_read_b128 v[194:197], v186 offset:1024
	ds_read_b128 v[198:201], v186 offset:2048
	ds_read_b128 v[202:205], v186 offset:3072
	ds_read_b128 v[206:209], v186 offset:4096
	ds_read_b128 v[210:213], v186 offset:5120
	ds_read_b128 v[220:223], v186 offset:6144
	ds_read_b128 v[224:227], v186 offset:7168
	global_load_lds_dwordx4 v[176:177], off
	v_lshl_add_u64 v[176:177], s[70:71], 0, v[170:171]
	s_add_i32 m0, s33, 0xe000
	s_nop 0
	global_load_lds_dwordx4 v[176:177], off
	s_waitcnt vmcnt(8)
	s_waitcnt lgkmcnt(0)
	s_barrier
	v_mfma_scale_f32_16x16x128_f8f6f4 v[158:161], v[26:33], v[190:197], v[158:161], v187, v188 op_sel_hi:[0,0,0]
	v_mfma_scale_f32_16x16x128_f8f6f4 v[154:157], v[18:25], v[190:197], v[154:157], v187, v188 op_sel_hi:[0,0,0]
	v_mfma_scale_f32_16x16x128_f8f6f4 v[150:153], v[26:33], v[198:205], v[150:153], v187, v188 op_sel_hi:[0,0,0]
	v_mfma_scale_f32_16x16x128_f8f6f4 v[142:145], v[18:25], v[198:205], v[142:145], v187, v188 op_sel_hi:[0,0,0]
	v_mfma_scale_f32_16x16x128_f8f6f4 v[134:137], v[26:33], v[206:213], v[134:137], v187, v188 op_sel_hi:[0,0,0]
	v_mfma_scale_f32_16x16x128_f8f6f4 v[126:129], v[18:25], v[206:213], v[126:129], v187, v188 op_sel_hi:[0,0,0]
	v_mfma_scale_f32_16x16x128_f8f6f4 v[118:121], v[26:33], v[220:227], v[118:121], v187, v188 op_sel_hi:[0,0,0]
	v_mfma_scale_f32_16x16x128_f8f6f4 v[110:113], v[18:25], v[220:227], v[110:113], v187, v188 op_sel_hi:[0,0,0]
	v_mfma_scale_f32_16x16x128_f8f6f4 v[146:149], v[10:17], v[190:197], v[146:149], v187, v188 op_sel_hi:[0,0,0]
	v_mfma_scale_f32_16x16x128_f8f6f4 v[138:141], v[2:9], v[190:197], v[138:141], v187, v188 op_sel_hi:[0,0,0]
	v_mfma_scale_f32_16x16x128_f8f6f4 v[130:133], v[10:17], v[198:205], v[130:133], v187, v188 op_sel_hi:[0,0,0]
	v_mfma_scale_f32_16x16x128_f8f6f4 v[122:125], v[2:9], v[198:205], v[122:125], v187, v188 op_sel_hi:[0,0,0]
	v_mfma_scale_f32_16x16x128_f8f6f4 v[114:117], v[10:17], v[206:213], v[114:117], v187, v188 op_sel_hi:[0,0,0]
	v_mfma_scale_f32_16x16x128_f8f6f4 v[106:109], v[2:9], v[206:213], v[106:109], v187, v188 op_sel_hi:[0,0,0]
	v_mfma_scale_f32_16x16x128_f8f6f4 v[102:105], v[10:17], v[220:227], v[102:105], v187, v188 op_sel_hi:[0,0,0]
	v_mfma_scale_f32_16x16x128_f8f6f4 v[98:101], v[2:9], v[220:227], v[98:101], v187, v188 op_sel_hi:[0,0,0]
	s_barrier
	s_add_i32 s26, s88, s80
	v_lshl_add_u64 v[176:177], s[74:75], 0, v[162:163]
	s_mov_b32 m0, s26
	ds_read_b128 v[190:193], v186 offset:16384
	ds_read_b128 v[194:197], v186 offset:17408
	ds_read_b128 v[198:201], v186 offset:18432
	ds_read_b128 v[202:205], v186 offset:19456
	ds_read_b128 v[206:209], v186 offset:20480
	ds_read_b128 v[210:213], v186 offset:21504
	ds_read_b128 v[220:223], v186 offset:22528
	ds_read_b128 v[224:227], v186 offset:23552
	global_load_lds_dwordx4 v[176:177], off
	v_lshl_add_u64 v[178:179], v[176:177], 0, s[8:9]
	s_add_i32 m0, s26, 0x2000
	s_add_i32 s26, s89, s80
	global_load_lds_dwordx4 v[178:179], off
	v_lshl_add_u64 v[178:179], v[176:177], 0, s[10:11]
	s_mov_b32 m0, s26
	v_lshl_add_u64 v[180:181], s[72:73], 0, v[166:167]
	global_load_lds_dwordx4 v[178:179], off
	v_lshl_add_u64 v[178:179], v[176:177], 0, s[12:13]
	s_add_i32 m0, s26, 0x2000
	s_nop 0
	global_load_lds_dwordx4 v[178:179], off
	v_lshl_add_u64 v[178:179], s[72:73], 0, v[164:165]
	s_mov_b32 m0, s33
	s_nop 0
	global_load_lds_dwordx4 v[178:179], off
	s_mov_b32 m0, s69
	s_nop 0
	global_load_lds_dwordx4 v[180:181], off
	s_waitcnt vmcnt(8)
	s_waitcnt lgkmcnt(0)
	s_barrier
	v_mfma_scale_f32_16x16x128_f8f6f4 v[94:97], v[26:33], v[190:197], v[94:97], v187, v188 op_sel_hi:[0,0,0]
	v_mfma_scale_f32_16x16x128_f8f6f4 v[90:93], v[18:25], v[190:197], v[90:93], v187, v188 op_sel_hi:[0,0,0]
	v_mfma_scale_f32_16x16x128_f8f6f4 v[86:89], v[26:33], v[198:205], v[86:89], v187, v188 op_sel_hi:[0,0,0]
	v_mfma_scale_f32_16x16x128_f8f6f4 v[78:81], v[18:25], v[198:205], v[78:81], v187, v188 op_sel_hi:[0,0,0]
	v_mfma_scale_f32_16x16x128_f8f6f4 v[70:73], v[26:33], v[206:213], v[70:73], v187, v188 op_sel_hi:[0,0,0]
	v_mfma_scale_f32_16x16x128_f8f6f4 v[62:65], v[18:25], v[206:213], v[62:65], v187, v188 op_sel_hi:[0,0,0]
	v_mfma_scale_f32_16x16x128_f8f6f4 v[54:57], v[26:33], v[220:227], v[54:57], v187, v188 op_sel_hi:[0,0,0]
	v_mfma_scale_f32_16x16x128_f8f6f4 v[46:49], v[18:25], v[220:227], v[46:49], v187, v188 op_sel_hi:[0,0,0]
	v_mfma_scale_f32_16x16x128_f8f6f4 v[82:85], v[10:17], v[190:197], v[82:85], v187, v188 op_sel_hi:[0,0,0]
	v_mfma_scale_f32_16x16x128_f8f6f4 v[74:77], v[2:9], v[190:197], v[74:77], v187, v188 op_sel_hi:[0,0,0]
	v_mfma_scale_f32_16x16x128_f8f6f4 v[66:69], v[10:17], v[198:205], v[66:69], v187, v188 op_sel_hi:[0,0,0]
	v_mfma_scale_f32_16x16x128_f8f6f4 v[58:61], v[2:9], v[198:205], v[58:61], v187, v188 op_sel_hi:[0,0,0]
	v_mfma_scale_f32_16x16x128_f8f6f4 v[50:53], v[10:17], v[206:213], v[50:53], v187, v188 op_sel_hi:[0,0,0]
	v_mfma_scale_f32_16x16x128_f8f6f4 v[42:45], v[2:9], v[206:213], v[42:45], v187, v188 op_sel_hi:[0,0,0]
	v_mfma_scale_f32_16x16x128_f8f6f4 v[38:41], v[10:17], v[220:227], v[38:41], v187, v188 op_sel_hi:[0,0,0]
	v_mfma_scale_f32_16x16x128_f8f6f4 v[34:37], v[2:9], v[220:227], v[34:37], v187, v188 op_sel_hi:[0,0,0]
	s_barrier
	s_add_i32 s74, 0, 0x18000
	s_add_i32 s75, 0, 0x1c000
	v_add_u32_e32 v14, s74, v183
	v_add_u32_e32 v30, s75, v183
	ds_read_b128 v[2:5], v14
	ds_read_b128 v[6:9], v14 offset:1024
	ds_read_b128 v[10:13], v14 offset:2048
	ds_read_b128 v[14:17], v14 offset:3072
	ds_read_b128 v[18:21], v30
	ds_read_b128 v[22:25], v30 offset:1024
	ds_read_b128 v[26:29], v30 offset:2048
	ds_read_b128 v[30:33], v30 offset:3072
	s_add_u32 s26, s72, 0x40000
	s_addc_u32 s27, s73, 0
	s_mov_b32 m0, s83
	v_lshl_add_u64 v[214:215], s[26:27], 0, v[164:165]
	ds_read_b128 v[190:193], v186 offset:32768
	ds_read_b128 v[194:197], v186 offset:33792
	ds_read_b128 v[198:201], v186 offset:34816
	ds_read_b128 v[202:205], v186 offset:35840
	ds_read_b128 v[206:209], v186 offset:36864
	ds_read_b128 v[210:213], v186 offset:37888
	ds_read_b128 v[220:223], v186 offset:38912
	ds_read_b128 v[224:227], v186 offset:39936
	global_load_lds_dwordx4 v[214:215], off
	v_lshl_add_u64 v[214:215], s[26:27], 0, v[166:167]
	s_mov_b32 m0, s84
	s_nop 0
	global_load_lds_dwordx4 v[214:215], off
	s_waitcnt vmcnt(8)
	s_waitcnt lgkmcnt(0)
	s_barrier
	v_mfma_scale_f32_16x16x128_f8f6f4 v[158:161], v[2:9], v[190:197], v[158:161], v187, v188 op_sel_hi:[0,0,0]
	v_mfma_scale_f32_16x16x128_f8f6f4 v[154:157], v[10:17], v[190:197], v[154:157], v187, v188 op_sel_hi:[0,0,0]
	v_mfma_scale_f32_16x16x128_f8f6f4 v[150:153], v[2:9], v[198:205], v[150:153], v187, v188 op_sel_hi:[0,0,0]
	v_mfma_scale_f32_16x16x128_f8f6f4 v[142:145], v[10:17], v[198:205], v[142:145], v187, v188 op_sel_hi:[0,0,0]
	v_mfma_scale_f32_16x16x128_f8f6f4 v[134:137], v[2:9], v[206:213], v[134:137], v187, v188 op_sel_hi:[0,0,0]
	v_mfma_scale_f32_16x16x128_f8f6f4 v[126:129], v[10:17], v[206:213], v[126:129], v187, v188 op_sel_hi:[0,0,0]
	v_mfma_scale_f32_16x16x128_f8f6f4 v[118:121], v[2:9], v[220:227], v[118:121], v187, v188 op_sel_hi:[0,0,0]
	v_mfma_scale_f32_16x16x128_f8f6f4 v[110:113], v[10:17], v[220:227], v[110:113], v187, v188 op_sel_hi:[0,0,0]
	v_mfma_scale_f32_16x16x128_f8f6f4 v[146:149], v[18:25], v[190:197], v[146:149], v187, v188 op_sel_hi:[0,0,0]
	v_mfma_scale_f32_16x16x128_f8f6f4 v[138:141], v[26:33], v[190:197], v[138:141], v187, v188 op_sel_hi:[0,0,0]
	v_mfma_scale_f32_16x16x128_f8f6f4 v[130:133], v[18:25], v[198:205], v[130:133], v187, v188 op_sel_hi:[0,0,0]
	v_mfma_scale_f32_16x16x128_f8f6f4 v[122:125], v[26:33], v[198:205], v[122:125], v187, v188 op_sel_hi:[0,0,0]
	v_mfma_scale_f32_16x16x128_f8f6f4 v[114:117], v[18:25], v[206:213], v[114:117], v187, v188 op_sel_hi:[0,0,0]
	v_mfma_scale_f32_16x16x128_f8f6f4 v[106:109], v[26:33], v[206:213], v[106:109], v187, v188 op_sel_hi:[0,0,0]
	v_mfma_scale_f32_16x16x128_f8f6f4 v[102:105], v[18:25], v[220:227], v[102:105], v187, v188 op_sel_hi:[0,0,0]
	v_mfma_scale_f32_16x16x128_f8f6f4 v[98:101], v[26:33], v[220:227], v[98:101], v187, v188 op_sel_hi:[0,0,0]
	s_barrier
	s_add_i32 s26, s74, s80
	v_lshl_add_u64 v[214:215], v[176:177], 0, s[16:17]
	s_mov_b32 m0, s26
	ds_read_b128 v[190:193], v186 offset:49152
	ds_read_b128 v[194:197], v186 offset:50176
	ds_read_b128 v[198:201], v186 offset:51200
	ds_read_b128 v[202:205], v186 offset:52224
	ds_read_b128 v[206:209], v186 offset:53248
	ds_read_b128 v[210:213], v186 offset:54272
	ds_read_b128 v[220:223], v186 offset:55296
	ds_read_b128 v[224:227], v186 offset:56320
	global_load_lds_dwordx4 v[214:215], off
	v_lshl_add_u64 v[214:215], v[176:177], 0, s[18:19]
	s_add_i32 m0, s26, 0x2000
	s_add_i32 s26, s75, s80
	global_load_lds_dwordx4 v[214:215], off
	v_lshl_add_u64 v[214:215], v[176:177], 0, s[22:23]
	s_mov_b32 m0, s26
	v_lshl_add_u64 v[176:177], v[176:177], 0, s[24:25]
	global_load_lds_dwordx4 v[214:215], off
	s_add_i32 m0, s26, 0x2000
	s_nop 0
	global_load_lds_dwordx4 v[176:177], off
	v_lshl_add_u64 v[176:177], v[178:179], 0, s[20:21]
	s_mov_b32 m0, s86
	s_nop 0
	global_load_lds_dwordx4 v[176:177], off
	v_lshl_add_u64 v[176:177], v[180:181], 0, s[20:21]
	s_mov_b32 m0, s87
	s_nop 0
	global_load_lds_dwordx4 v[176:177], off
	s_waitcnt vmcnt(8)
	s_waitcnt lgkmcnt(0)
	s_barrier
	v_mfma_scale_f32_16x16x128_f8f6f4 v[94:97], v[2:9], v[190:197], v[94:97], v187, v188 op_sel_hi:[0,0,0]
	v_mfma_scale_f32_16x16x128_f8f6f4 v[90:93], v[10:17], v[190:197], v[90:93], v187, v188 op_sel_hi:[0,0,0]
	v_mfma_scale_f32_16x16x128_f8f6f4 v[86:89], v[2:9], v[198:205], v[86:89], v187, v188 op_sel_hi:[0,0,0]
	v_mfma_scale_f32_16x16x128_f8f6f4 v[78:81], v[10:17], v[198:205], v[78:81], v187, v188 op_sel_hi:[0,0,0]
	v_mfma_scale_f32_16x16x128_f8f6f4 v[70:73], v[2:9], v[206:213], v[70:73], v187, v188 op_sel_hi:[0,0,0]
	v_mfma_scale_f32_16x16x128_f8f6f4 v[62:65], v[10:17], v[206:213], v[62:65], v187, v188 op_sel_hi:[0,0,0]
	v_mfma_scale_f32_16x16x128_f8f6f4 v[54:57], v[2:9], v[220:227], v[54:57], v187, v188 op_sel_hi:[0,0,0]
	v_mfma_scale_f32_16x16x128_f8f6f4 v[46:49], v[10:17], v[220:227], v[46:49], v187, v188 op_sel_hi:[0,0,0]
	v_mfma_scale_f32_16x16x128_f8f6f4 v[82:85], v[18:25], v[190:197], v[82:85], v187, v188 op_sel_hi:[0,0,0]
	v_mfma_scale_f32_16x16x128_f8f6f4 v[74:77], v[26:33], v[190:197], v[74:77], v187, v188 op_sel_hi:[0,0,0]
	v_mfma_scale_f32_16x16x128_f8f6f4 v[66:69], v[18:25], v[198:205], v[66:69], v187, v188 op_sel_hi:[0,0,0]
	v_mfma_scale_f32_16x16x128_f8f6f4 v[58:61], v[26:33], v[198:205], v[58:61], v187, v188 op_sel_hi:[0,0,0]
	v_mfma_scale_f32_16x16x128_f8f6f4 v[50:53], v[18:25], v[206:213], v[50:53], v187, v188 op_sel_hi:[0,0,0]
	v_mfma_scale_f32_16x16x128_f8f6f4 v[42:45], v[26:33], v[206:213], v[42:45], v187, v188 op_sel_hi:[0,0,0]
	v_mfma_scale_f32_16x16x128_f8f6f4 v[38:41], v[18:25], v[220:227], v[38:41], v187, v188 op_sel_hi:[0,0,0]
	v_mfma_scale_f32_16x16x128_f8f6f4 v[34:37], v[26:33], v[220:227], v[34:37], v187, v188 op_sel_hi:[0,0,0]
	s_barrier
	s_add_i32 s94, s94, 2
	s_add_u32 s92, s92, 0x10000
	s_addc_u32 s93, s93, 0
	s_add_u32 s70, s70, 0x100
	s_addc_u32 s71, s71, 0
	s_cmp_gt_u32 s94, 13
	s_cbranch_scc0 .LBB0_285
	s_and_b64 vcc, exec, s[40:41]
	s_cbranch_vccz .LBB0_288
	s_barrier

.LBB0_660:
	ds_read_b128 v[130:133], v222
	ds_read_b128 v[134:137], v222 offset:1024
	ds_read_b128 v[138:141], v222 offset:2048
	ds_read_b128 v[142:145], v222 offset:3072
	ds_read_b128 v[146:149], v223
	ds_read_b128 v[150:153], v223 offset:1024
	ds_read_b128 v[154:157], v223 offset:2048
	ds_read_b128 v[158:161], v223 offset:3072
	s_add_u32 s26, s58, 0xfff80080
	s_addc_u32 s27, s59, -1
	s_cmp_eq_u32 s80, 28
	s_cselect_b32 s61, s45, s27
	s_cselect_b32 s60, s72, s26
	s_cselect_b32 s27, s41, s75
	s_cselect_b32 s26, s73, s74
	v_lshl_add_u64 v[208:209], s[58:59], 0, v[200:201]
	s_add_i32 m0, s57, 0xc000
	ds_read_b128 v[162:165], v224
	ds_read_b128 v[166:169], v224 offset:1024
	ds_read_b128 v[170:173], v224 offset:2048
	ds_read_b128 v[174:177], v224 offset:3072
	ds_read_b128 v[178:181], v224 offset:4096
	ds_read_b128 v[182:185], v224 offset:5120
	ds_read_b128 v[186:189], v224 offset:6144
	ds_read_b128 v[190:193], v224 offset:7168
	global_load_lds_dwordx4 v[208:209], off
	v_lshl_add_u64 v[208:209], s[58:59], 0, v[202:203]
	s_add_i32 m0, s57, 0xe000
	s_nop 0
	global_load_lds_dwordx4 v[208:209], off
	s_waitcnt vmcnt(8)
	s_waitcnt lgkmcnt(0)
	s_barrier
	v_mfma_f32_16x16x32_bf16 v[126:129], v[130:133], v[162:165], v[126:129]
	v_mfma_f32_16x16x32_bf16 v[122:125], v[138:141], v[162:165], v[122:125]
	v_mfma_f32_16x16x32_bf16 v[118:121], v[130:133], v[170:173], v[118:121]
	v_mfma_f32_16x16x32_bf16 v[114:117], v[138:141], v[170:173], v[114:117]
	v_mfma_f32_16x16x32_bf16 v[110:113], v[130:133], v[178:181], v[110:113]
	v_mfma_f32_16x16x32_bf16 v[102:105], v[138:141], v[178:181], v[102:105]
	v_mfma_f32_16x16x32_bf16 v[94:97], v[130:133], v[186:189], v[94:97]
	v_mfma_f32_16x16x32_bf16 v[74:77], v[138:141], v[186:189], v[74:77]
	v_mfma_f32_16x16x32_bf16 v[126:129], v[134:137], v[166:169], v[126:129]
	v_mfma_f32_16x16x32_bf16 v[122:125], v[142:145], v[166:169], v[122:125]
	v_mfma_f32_16x16x32_bf16 v[118:121], v[134:137], v[174:177], v[118:121]
	v_mfma_f32_16x16x32_bf16 v[114:117], v[142:145], v[174:177], v[114:117]
	v_mfma_f32_16x16x32_bf16 v[110:113], v[134:137], v[182:185], v[110:113]
	v_mfma_f32_16x16x32_bf16 v[102:105], v[142:145], v[182:185], v[102:105]
	v_mfma_f32_16x16x32_bf16 v[94:97], v[134:137], v[190:193], v[94:97]
	v_mfma_f32_16x16x32_bf16 v[74:77], v[142:145], v[190:193], v[74:77]
	v_mfma_f32_16x16x32_bf16 v[106:109], v[146:149], v[162:165], v[106:109]
	v_mfma_f32_16x16x32_bf16 v[98:101], v[154:157], v[162:165], v[98:101]
	v_mfma_f32_16x16x32_bf16 v[90:93], v[146:149], v[170:173], v[90:93]
	v_mfma_f32_16x16x32_bf16 v[86:89], v[154:157], v[170:173], v[86:89]
	v_mfma_f32_16x16x32_bf16 v[82:85], v[146:149], v[178:181], v[82:85]
	v_mfma_f32_16x16x32_bf16 v[78:81], v[154:157], v[178:181], v[78:81]
	v_mfma_f32_16x16x32_bf16 v[70:73], v[146:149], v[186:189], v[70:73]
	v_mfma_f32_16x16x32_bf16 v[66:69], v[154:157], v[186:189], v[66:69]
	v_mfma_f32_16x16x32_bf16 v[106:109], v[150:153], v[166:169], v[106:109]
	v_mfma_f32_16x16x32_bf16 v[98:101], v[158:161], v[166:169], v[98:101]
	v_mfma_f32_16x16x32_bf16 v[90:93], v[150:153], v[174:177], v[90:93]
	v_mfma_f32_16x16x32_bf16 v[86:89], v[158:161], v[174:177], v[86:89]
	v_mfma_f32_16x16x32_bf16 v[82:85], v[150:153], v[182:185], v[82:85]
	v_mfma_f32_16x16x32_bf16 v[78:81], v[158:161], v[182:185], v[78:81]
	v_mfma_f32_16x16x32_bf16 v[70:73], v[150:153], v[190:193], v[70:73]
	v_mfma_f32_16x16x32_bf16 v[66:69], v[158:161], v[190:193], v[66:69]
	s_barrier
	v_lshl_add_u64 v[208:209], s[26:27], 0, v[194:195]
	s_add_i32 s26, s70, s35
	s_mov_b32 m0, s26
	ds_read_b128 v[162:165], v224 offset:16384
	ds_read_b128 v[166:169], v224 offset:17408
	ds_read_b128 v[170:173], v224 offset:18432
	ds_read_b128 v[174:177], v224 offset:19456
	ds_read_b128 v[178:181], v224 offset:20480
	ds_read_b128 v[182:185], v224 offset:21504
	ds_read_b128 v[186:189], v224 offset:22528
	ds_read_b128 v[190:193], v224 offset:23552
	global_load_lds_dwordx4 v[208:209], off
	v_lshl_add_u64 v[210:211], v[208:209], 0, s[6:7]
	s_add_i32 m0, s26, 0x2000
	s_add_i32 s26, s71, s35
	global_load_lds_dwordx4 v[210:211], off
	v_lshl_add_u64 v[210:211], v[208:209], 0, s[8:9]
	s_mov_b32 m0, s26
	v_lshl_add_u64 v[212:213], s[60:61], 0, v[198:199]
	global_load_lds_dwordx4 v[210:211], off
	v_lshl_add_u64 v[210:211], v[208:209], 0, s[10:11]
	s_add_i32 m0, s26, 0x2000
	s_nop 0
	global_load_lds_dwordx4 v[210:211], off
	v_lshl_add_u64 v[210:211], s[60:61], 0, v[196:197]
	s_mov_b32 m0, s57
	s_nop 0
	global_load_lds_dwordx4 v[210:211], off
	s_mov_b32 m0, s63
	s_nop 0
	global_load_lds_dwordx4 v[212:213], off
	s_waitcnt vmcnt(8)
	s_waitcnt lgkmcnt(0)
	s_barrier
	v_mfma_f32_16x16x32_bf16 v[62:65], v[130:133], v[162:165], v[62:65]
	v_mfma_f32_16x16x32_bf16 v[58:61], v[138:141], v[162:165], v[58:61]
	v_mfma_f32_16x16x32_bf16 v[54:57], v[130:133], v[170:173], v[54:57]
	v_mfma_f32_16x16x32_bf16 v[50:53], v[138:141], v[170:173], v[50:53]
	v_mfma_f32_16x16x32_bf16 v[46:49], v[130:133], v[178:181], v[46:49]
	v_mfma_f32_16x16x32_bf16 v[38:41], v[138:141], v[178:181], v[38:41]
	v_mfma_f32_16x16x32_bf16 v[30:33], v[130:133], v[186:189], v[30:33]
	v_mfma_f32_16x16x32_bf16 v[10:13], v[138:141], v[186:189], v[10:13]
	v_mfma_f32_16x16x32_bf16 v[62:65], v[134:137], v[166:169], v[62:65]
	v_mfma_f32_16x16x32_bf16 v[58:61], v[142:145], v[166:169], v[58:61]
	v_mfma_f32_16x16x32_bf16 v[54:57], v[134:137], v[174:177], v[54:57]
	v_mfma_f32_16x16x32_bf16 v[50:53], v[142:145], v[174:177], v[50:53]
	v_mfma_f32_16x16x32_bf16 v[46:49], v[134:137], v[182:185], v[46:49]
	v_mfma_f32_16x16x32_bf16 v[38:41], v[142:145], v[182:185], v[38:41]
	v_mfma_f32_16x16x32_bf16 v[30:33], v[134:137], v[190:193], v[30:33]
	v_mfma_f32_16x16x32_bf16 v[10:13], v[142:145], v[190:193], v[10:13]
	v_mfma_f32_16x16x32_bf16 v[42:45], v[146:149], v[162:165], v[42:45]
	v_mfma_f32_16x16x32_bf16 v[34:37], v[154:157], v[162:165], v[34:37]
	v_mfma_f32_16x16x32_bf16 v[26:29], v[146:149], v[170:173], v[26:29]
	v_mfma_f32_16x16x32_bf16 v[22:25], v[154:157], v[170:173], v[22:25]
	v_mfma_f32_16x16x32_bf16 v[18:21], v[146:149], v[178:181], v[18:21]
	v_mfma_f32_16x16x32_bf16 v[14:17], v[154:157], v[178:181], v[14:17]
	v_mfma_f32_16x16x32_bf16 v[6:9], v[146:149], v[186:189], v[6:9]
	v_mfma_f32_16x16x32_bf16 v[2:5], v[154:157], v[186:189], v[2:5]
	v_mfma_f32_16x16x32_bf16 v[42:45], v[150:153], v[166:169], v[42:45]
	v_mfma_f32_16x16x32_bf16 v[34:37], v[158:161], v[166:169], v[34:37]
	v_mfma_f32_16x16x32_bf16 v[26:29], v[150:153], v[174:177], v[26:29]
	v_mfma_f32_16x16x32_bf16 v[22:25], v[158:161], v[174:177], v[22:25]
	v_mfma_f32_16x16x32_bf16 v[18:21], v[150:153], v[182:185], v[18:21]
	v_mfma_f32_16x16x32_bf16 v[14:17], v[158:161], v[182:185], v[14:17]
	v_mfma_f32_16x16x32_bf16 v[6:9], v[150:153], v[190:193], v[6:9]
	v_mfma_f32_16x16x32_bf16 v[2:5], v[158:161], v[190:193], v[2:5]
	s_barrier
	s_add_i32 s81, 0, 0x18000
	s_add_i32 s82, 0, 0x1c000
	v_add_u32_e32 v142, s81, v220
	v_add_u32_e32 v158, s82, v220
	ds_read_b128 v[130:133], v142
	ds_read_b128 v[134:137], v142 offset:1024
	ds_read_b128 v[138:141], v142 offset:2048
	ds_read_b128 v[142:145], v142 offset:3072
	ds_read_b128 v[146:149], v158
	ds_read_b128 v[150:153], v158 offset:1024
	ds_read_b128 v[154:157], v158 offset:2048
	ds_read_b128 v[158:161], v158 offset:3072
	s_add_u32 s26, s60, 0x80000
	s_addc_u32 s27, s61, 0
	s_mov_b32 m0, s64
	v_lshl_add_u64 v[214:215], s[26:27], 0, v[196:197]
	ds_read_b128 v[162:165], v224 offset:32768
	ds_read_b128 v[166:169], v224 offset:33792
	ds_read_b128 v[170:173], v224 offset:34816
	ds_read_b128 v[174:177], v224 offset:35840
	ds_read_b128 v[178:181], v224 offset:36864
	ds_read_b128 v[182:185], v224 offset:37888
	ds_read_b128 v[186:189], v224 offset:38912
	ds_read_b128 v[190:193], v224 offset:39936
	global_load_lds_dwordx4 v[214:215], off
	v_lshl_add_u64 v[214:215], s[26:27], 0, v[198:199]
	s_mov_b32 m0, s65
	s_nop 0
	global_load_lds_dwordx4 v[214:215], off
	s_waitcnt vmcnt(8)
	s_waitcnt lgkmcnt(0)
	s_barrier
	v_mfma_f32_16x16x32_bf16 v[126:129], v[130:133], v[162:165], v[126:129]
	v_mfma_f32_16x16x32_bf16 v[122:125], v[138:141], v[162:165], v[122:125]
	v_mfma_f32_16x16x32_bf16 v[118:121], v[130:133], v[170:173], v[118:121]
	v_mfma_f32_16x16x32_bf16 v[114:117], v[138:141], v[170:173], v[114:117]
	v_mfma_f32_16x16x32_bf16 v[110:113], v[130:133], v[178:181], v[110:113]
	v_mfma_f32_16x16x32_bf16 v[102:105], v[138:141], v[178:181], v[102:105]
	v_mfma_f32_16x16x32_bf16 v[94:97], v[130:133], v[186:189], v[94:97]
	v_mfma_f32_16x16x32_bf16 v[74:77], v[138:141], v[186:189], v[74:77]
	v_mfma_f32_16x16x32_bf16 v[126:129], v[134:137], v[166:169], v[126:129]
	v_mfma_f32_16x16x32_bf16 v[122:125], v[142:145], v[166:169], v[122:125]
	v_mfma_f32_16x16x32_bf16 v[118:121], v[134:137], v[174:177], v[118:121]
	v_mfma_f32_16x16x32_bf16 v[114:117], v[142:145], v[174:177], v[114:117]
	v_mfma_f32_16x16x32_bf16 v[110:113], v[134:137], v[182:185], v[110:113]
	v_mfma_f32_16x16x32_bf16 v[102:105], v[142:145], v[182:185], v[102:105]
	v_mfma_f32_16x16x32_bf16 v[94:97], v[134:137], v[190:193], v[94:97]
	v_mfma_f32_16x16x32_bf16 v[74:77], v[142:145], v[190:193], v[74:77]
	v_mfma_f32_16x16x32_bf16 v[106:109], v[146:149], v[162:165], v[106:109]
	v_mfma_f32_16x16x32_bf16 v[98:101], v[154:157], v[162:165], v[98:101]
	v_mfma_f32_16x16x32_bf16 v[90:93], v[146:149], v[170:173], v[90:93]
	v_mfma_f32_16x16x32_bf16 v[86:89], v[154:157], v[170:173], v[86:89]
	v_mfma_f32_16x16x32_bf16 v[82:85], v[146:149], v[178:181], v[82:85]
	v_mfma_f32_16x16x32_bf16 v[78:81], v[154:157], v[178:181], v[78:81]
	v_mfma_f32_16x16x32_bf16 v[70:73], v[146:149], v[186:189], v[70:73]
	v_mfma_f32_16x16x32_bf16 v[66:69], v[154:157], v[186:189], v[66:69]
	v_mfma_f32_16x16x32_bf16 v[106:109], v[150:153], v[166:169], v[106:109]
	v_mfma_f32_16x16x32_bf16 v[98:101], v[158:161], v[166:169], v[98:101]
	v_mfma_f32_16x16x32_bf16 v[90:93], v[150:153], v[174:177], v[90:93]
	v_mfma_f32_16x16x32_bf16 v[86:89], v[158:161], v[174:177], v[86:89]
	v_mfma_f32_16x16x32_bf16 v[82:85], v[150:153], v[182:185], v[82:85]
	v_mfma_f32_16x16x32_bf16 v[78:81], v[158:161], v[182:185], v[78:81]
	v_mfma_f32_16x16x32_bf16 v[70:73], v[150:153], v[190:193], v[70:73]
	v_mfma_f32_16x16x32_bf16 v[66:69], v[158:161], v[190:193], v[66:69]
	s_barrier
	s_add_i32 s26, s81, s35
	v_lshl_add_u64 v[214:215], v[208:209], 0, s[14:15]
	s_mov_b32 m0, s26
	ds_read_b128 v[162:165], v224 offset:49152
	ds_read_b128 v[166:169], v224 offset:50176
	ds_read_b128 v[170:173], v224 offset:51200
	ds_read_b128 v[174:177], v224 offset:52224
	ds_read_b128 v[178:181], v224 offset:53248
	ds_read_b128 v[182:185], v224 offset:54272
	ds_read_b128 v[186:189], v224 offset:55296
	ds_read_b128 v[190:193], v224 offset:56320
	global_load_lds_dwordx4 v[214:215], off
	v_lshl_add_u64 v[214:215], v[208:209], 0, s[16:17]
	s_add_i32 m0, s26, 0x2000
	s_add_i32 s26, s82, s35
	global_load_lds_dwordx4 v[214:215], off
	v_lshl_add_u64 v[214:215], v[208:209], 0, s[20:21]
	s_mov_b32 m0, s26
	v_lshl_add_u64 v[208:209], v[208:209], 0, s[22:23]
	global_load_lds_dwordx4 v[214:215], off
	s_add_i32 m0, s26, 0x2000
	s_nop 0
	global_load_lds_dwordx4 v[208:209], off
	v_lshl_add_u64 v[208:209], v[210:211], 0, s[18:19]
	s_mov_b32 m0, s67
	s_nop 0
	global_load_lds_dwordx4 v[208:209], off
	v_lshl_add_u64 v[208:209], v[212:213], 0, s[18:19]
	s_mov_b32 m0, s68
	s_nop 0
	global_load_lds_dwordx4 v[208:209], off
	s_waitcnt vmcnt(8)
	s_waitcnt lgkmcnt(0)
	s_barrier
	v_mfma_f32_16x16x32_bf16 v[62:65], v[130:133], v[162:165], v[62:65]
	v_mfma_f32_16x16x32_bf16 v[58:61], v[138:141], v[162:165], v[58:61]
	v_mfma_f32_16x16x32_bf16 v[54:57], v[130:133], v[170:173], v[54:57]
	v_mfma_f32_16x16x32_bf16 v[50:53], v[138:141], v[170:173], v[50:53]
	v_mfma_f32_16x16x32_bf16 v[46:49], v[130:133], v[178:181], v[46:49]
	v_mfma_f32_16x16x32_bf16 v[38:41], v[138:141], v[178:181], v[38:41]
	v_mfma_f32_16x16x32_bf16 v[30:33], v[130:133], v[186:189], v[30:33]
	v_mfma_f32_16x16x32_bf16 v[10:13], v[138:141], v[186:189], v[10:13]
	v_mfma_f32_16x16x32_bf16 v[62:65], v[134:137], v[166:169], v[62:65]
	v_mfma_f32_16x16x32_bf16 v[58:61], v[142:145], v[166:169], v[58:61]
	v_mfma_f32_16x16x32_bf16 v[54:57], v[134:137], v[174:177], v[54:57]
	v_mfma_f32_16x16x32_bf16 v[50:53], v[142:145], v[174:177], v[50:53]
	v_mfma_f32_16x16x32_bf16 v[46:49], v[134:137], v[182:185], v[46:49]
	v_mfma_f32_16x16x32_bf16 v[38:41], v[142:145], v[182:185], v[38:41]
	v_mfma_f32_16x16x32_bf16 v[30:33], v[134:137], v[190:193], v[30:33]
	v_mfma_f32_16x16x32_bf16 v[10:13], v[142:145], v[190:193], v[10:13]
	v_mfma_f32_16x16x32_bf16 v[42:45], v[146:149], v[162:165], v[42:45]
	v_mfma_f32_16x16x32_bf16 v[34:37], v[154:157], v[162:165], v[34:37]
	v_mfma_f32_16x16x32_bf16 v[26:29], v[146:149], v[170:173], v[26:29]
	v_mfma_f32_16x16x32_bf16 v[22:25], v[154:157], v[170:173], v[22:25]
	v_mfma_f32_16x16x32_bf16 v[18:21], v[146:149], v[178:181], v[18:21]
	v_mfma_f32_16x16x32_bf16 v[14:17], v[154:157], v[178:181], v[14:17]
	v_mfma_f32_16x16x32_bf16 v[6:9], v[146:149], v[186:189], v[6:9]
	v_mfma_f32_16x16x32_bf16 v[2:5], v[154:157], v[186:189], v[2:5]
	v_mfma_f32_16x16x32_bf16 v[42:45], v[150:153], v[166:169], v[42:45]
	v_mfma_f32_16x16x32_bf16 v[34:37], v[158:161], v[166:169], v[34:37]
	v_mfma_f32_16x16x32_bf16 v[26:29], v[150:153], v[174:177], v[26:29]
	v_mfma_f32_16x16x32_bf16 v[22:25], v[158:161], v[174:177], v[22:25]
	v_mfma_f32_16x16x32_bf16 v[18:21], v[150:153], v[182:185], v[18:21]
	v_mfma_f32_16x16x32_bf16 v[14:17], v[158:161], v[182:185], v[14:17]
	v_mfma_f32_16x16x32_bf16 v[6:9], v[150:153], v[190:193], v[6:9]
	v_mfma_f32_16x16x32_bf16 v[2:5], v[158:161], v[190:193], v[2:5]
	s_barrier
	s_add_i32 s80, s80, 2
	s_add_u32 s74, s74, 0x10000
	s_addc_u32 s75, s75, 0
	s_add_u32 s58, s58, 0x100
	s_addc_u32 s59, s59, 0
	s_cmp_gt_u32 s80, 29
	s_cbranch_scc0 .LBB0_660
	s_and_b64 vcc, exec, s[24:25]
	s_cbranch_vccz .LBB0_663
	s_barrier

.LBB0_783:
	ds_read_b128 v[144:147], v151
	ds_read_b128 v[156:159], v151 offset:1024
	ds_read_b128 v[160:163], v151 offset:2048
	ds_read_b128 v[164:167], v151 offset:3072
	ds_read_b128 v[168:171], v152
	ds_read_b128 v[172:175], v152 offset:1024
	ds_read_b128 v[176:179], v152 offset:2048
	ds_read_b128 v[180:183], v152 offset:3072
	s_add_u32 s26, s62, 0xfff80080
	s_addc_u32 s27, s63, -1
	s_cmp_eq_u32 s85, 28
	s_cselect_b32 s65, s55, s27
	s_cselect_b32 s64, s81, s26
	s_cselect_b32 s27, s53, s84
	s_cselect_b32 s26, s82, s83
	v_lshl_add_u64 v[216:217], s[62:63], 0, v[136:137]
	s_add_i32 m0, s61, 0xc000
	ds_read_b128 v[184:187], v153
	ds_read_b128 v[188:191], v153 offset:1024
	ds_read_b128 v[192:195], v153 offset:2048
	ds_read_b128 v[196:199], v153 offset:3072
	ds_read_b128 v[200:203], v153 offset:4096
	ds_read_b128 v[204:207], v153 offset:5120
	ds_read_b128 v[208:211], v153 offset:6144
	ds_read_b128 v[212:215], v153 offset:7168
	global_load_lds_dwordx4 v[216:217], off
	v_lshl_add_u64 v[216:217], s[62:63], 0, v[138:139]
	s_add_i32 m0, s61, 0xe000
	s_nop 0
	global_load_lds_dwordx4 v[216:217], off
	s_waitcnt vmcnt(8)
	s_waitcnt lgkmcnt(0)
	s_barrier
	v_mfma_f32_16x16x32_bf16 v[126:129], v[144:147], v[184:187], v[126:129]
	v_mfma_f32_16x16x32_bf16 v[118:121], v[160:163], v[184:187], v[118:121]
	v_mfma_f32_16x16x32_bf16 v[110:113], v[144:147], v[192:195], v[110:113]
	v_mfma_f32_16x16x32_bf16 v[102:105], v[160:163], v[192:195], v[102:105]
	v_mfma_f32_16x16x32_bf16 v[94:97], v[144:147], v[200:203], v[94:97]
	v_mfma_f32_16x16x32_bf16 v[86:89], v[160:163], v[200:203], v[86:89]
	v_mfma_f32_16x16x32_bf16 v[78:81], v[144:147], v[208:211], v[78:81]
	v_mfma_f32_16x16x32_bf16 v[70:73], v[160:163], v[208:211], v[70:73]
	v_mfma_f32_16x16x32_bf16 v[126:129], v[156:159], v[188:191], v[126:129]
	v_mfma_f32_16x16x32_bf16 v[118:121], v[164:167], v[188:191], v[118:121]
	v_mfma_f32_16x16x32_bf16 v[110:113], v[156:159], v[196:199], v[110:113]
	v_mfma_f32_16x16x32_bf16 v[102:105], v[164:167], v[196:199], v[102:105]
	v_mfma_f32_16x16x32_bf16 v[94:97], v[156:159], v[204:207], v[94:97]
	v_mfma_f32_16x16x32_bf16 v[86:89], v[164:167], v[204:207], v[86:89]
	v_mfma_f32_16x16x32_bf16 v[78:81], v[156:159], v[212:215], v[78:81]
	v_mfma_f32_16x16x32_bf16 v[70:73], v[164:167], v[212:215], v[70:73]
	v_mfma_f32_16x16x32_bf16 v[122:125], v[168:171], v[184:187], v[122:125]
	v_mfma_f32_16x16x32_bf16 v[114:117], v[176:179], v[184:187], v[114:117]
	v_mfma_f32_16x16x32_bf16 v[106:109], v[168:171], v[192:195], v[106:109]
	v_mfma_f32_16x16x32_bf16 v[98:101], v[176:179], v[192:195], v[98:101]
	v_mfma_f32_16x16x32_bf16 v[90:93], v[168:171], v[200:203], v[90:93]
	v_mfma_f32_16x16x32_bf16 v[82:85], v[176:179], v[200:203], v[82:85]
	v_mfma_f32_16x16x32_bf16 v[74:77], v[168:171], v[208:211], v[74:77]
	v_mfma_f32_16x16x32_bf16 v[66:69], v[176:179], v[208:211], v[66:69]
	v_mfma_f32_16x16x32_bf16 v[122:125], v[172:175], v[188:191], v[122:125]
	v_mfma_f32_16x16x32_bf16 v[114:117], v[180:183], v[188:191], v[114:117]
	v_mfma_f32_16x16x32_bf16 v[106:109], v[172:175], v[196:199], v[106:109]
	v_mfma_f32_16x16x32_bf16 v[98:101], v[180:183], v[196:199], v[98:101]
	v_mfma_f32_16x16x32_bf16 v[90:93], v[172:175], v[204:207], v[90:93]
	v_mfma_f32_16x16x32_bf16 v[82:85], v[180:183], v[204:207], v[82:85]
	v_mfma_f32_16x16x32_bf16 v[74:77], v[172:175], v[212:215], v[74:77]
	v_mfma_f32_16x16x32_bf16 v[66:69], v[180:183], v[212:215], v[66:69]
	s_barrier
	v_lshl_add_u64 v[216:217], s[26:27], 0, v[130:131]
	s_add_i32 s26, s73, s35
	s_mov_b32 m0, s26
	ds_read_b128 v[184:187], v153 offset:16384
	ds_read_b128 v[188:191], v153 offset:17408
	ds_read_b128 v[192:195], v153 offset:18432
	ds_read_b128 v[196:199], v153 offset:19456
	ds_read_b128 v[200:203], v153 offset:20480
	ds_read_b128 v[204:207], v153 offset:21504
	ds_read_b128 v[208:211], v153 offset:22528
	ds_read_b128 v[212:215], v153 offset:23552
	global_load_lds_dwordx4 v[216:217], off
	v_lshl_add_u64 v[220:221], v[216:217], 0, s[6:7]
	s_add_i32 m0, s26, 0x2000
	s_add_i32 s26, s74, s35
	global_load_lds_dwordx4 v[220:221], off
	v_lshl_add_u64 v[220:221], v[216:217], 0, s[8:9]
	s_mov_b32 m0, s26
	v_lshl_add_u64 v[222:223], s[64:65], 0, v[134:135]
	global_load_lds_dwordx4 v[220:221], off
	v_lshl_add_u64 v[220:221], v[216:217], 0, s[10:11]
	s_add_i32 m0, s26, 0x2000
	s_nop 0
	global_load_lds_dwordx4 v[220:221], off
	v_lshl_add_u64 v[220:221], s[64:65], 0, v[132:133]
	s_mov_b32 m0, s61
	s_nop 0
	global_load_lds_dwordx4 v[220:221], off
	s_mov_b32 m0, s66
	s_nop 0
	global_load_lds_dwordx4 v[222:223], off
	s_waitcnt vmcnt(8)
	s_waitcnt lgkmcnt(0)
	s_barrier
	v_mfma_f32_16x16x32_bf16 v[62:65], v[144:147], v[184:187], v[62:65]
	v_mfma_f32_16x16x32_bf16 v[54:57], v[160:163], v[184:187], v[54:57]
	v_mfma_f32_16x16x32_bf16 v[46:49], v[144:147], v[192:195], v[46:49]
	v_mfma_f32_16x16x32_bf16 v[38:41], v[160:163], v[192:195], v[38:41]
	v_mfma_f32_16x16x32_bf16 v[30:33], v[144:147], v[200:203], v[30:33]
	v_mfma_f32_16x16x32_bf16 v[22:25], v[160:163], v[200:203], v[22:25]
	v_mfma_f32_16x16x32_bf16 v[14:17], v[144:147], v[208:211], v[14:17]
	v_mfma_f32_16x16x32_bf16 v[6:9], v[160:163], v[208:211], v[6:9]
	v_mfma_f32_16x16x32_bf16 v[62:65], v[156:159], v[188:191], v[62:65]
	v_mfma_f32_16x16x32_bf16 v[54:57], v[164:167], v[188:191], v[54:57]
	v_mfma_f32_16x16x32_bf16 v[46:49], v[156:159], v[196:199], v[46:49]
	v_mfma_f32_16x16x32_bf16 v[38:41], v[164:167], v[196:199], v[38:41]
	v_mfma_f32_16x16x32_bf16 v[30:33], v[156:159], v[204:207], v[30:33]
	v_mfma_f32_16x16x32_bf16 v[22:25], v[164:167], v[204:207], v[22:25]
	v_mfma_f32_16x16x32_bf16 v[14:17], v[156:159], v[212:215], v[14:17]
	v_mfma_f32_16x16x32_bf16 v[6:9], v[164:167], v[212:215], v[6:9]
	v_mfma_f32_16x16x32_bf16 v[58:61], v[168:171], v[184:187], v[58:61]
	v_mfma_f32_16x16x32_bf16 v[50:53], v[176:179], v[184:187], v[50:53]
	v_mfma_f32_16x16x32_bf16 v[42:45], v[168:171], v[192:195], v[42:45]
	v_mfma_f32_16x16x32_bf16 v[34:37], v[176:179], v[192:195], v[34:37]
	v_mfma_f32_16x16x32_bf16 v[26:29], v[168:171], v[200:203], v[26:29]
	v_mfma_f32_16x16x32_bf16 v[18:21], v[176:179], v[200:203], v[18:21]
	v_mfma_f32_16x16x32_bf16 v[10:13], v[168:171], v[208:211], v[10:13]
	v_mfma_f32_16x16x32_bf16 v[2:5], v[176:179], v[208:211], v[2:5]
	v_mfma_f32_16x16x32_bf16 v[58:61], v[172:175], v[188:191], v[58:61]
	v_mfma_f32_16x16x32_bf16 v[50:53], v[180:183], v[188:191], v[50:53]
	v_mfma_f32_16x16x32_bf16 v[42:45], v[172:175], v[196:199], v[42:45]
	v_mfma_f32_16x16x32_bf16 v[34:37], v[180:183], v[196:199], v[34:37]
	v_mfma_f32_16x16x32_bf16 v[26:29], v[172:175], v[204:207], v[26:29]
	v_mfma_f32_16x16x32_bf16 v[18:21], v[180:183], v[204:207], v[18:21]
	v_mfma_f32_16x16x32_bf16 v[10:13], v[172:175], v[212:215], v[10:13]
	v_mfma_f32_16x16x32_bf16 v[2:5], v[180:183], v[212:215], v[2:5]
	s_barrier
	s_add_i32 s86, 0, 0x18000
	v_add_u32_e32 v155, s86, v149
	s_add_i32 s87, 0, 0x1c000
	ds_read_b128 v[144:147], v155
	ds_read_b128 v[156:159], v155 offset:1024
	ds_read_b128 v[160:163], v155 offset:2048
	ds_read_b128 v[164:167], v155 offset:3072
	v_add_u32_e32 v155, s87, v149
	ds_read_b128 v[168:171], v155
	ds_read_b128 v[172:175], v155 offset:1024
	ds_read_b128 v[176:179], v155 offset:2048
	ds_read_b128 v[180:183], v155 offset:3072
	s_add_u32 s26, s64, 0x80000
	s_addc_u32 s27, s65, 0
	s_mov_b32 m0, s67
	v_lshl_add_u64 v[224:225], s[26:27], 0, v[132:133]
	ds_read_b128 v[184:187], v153 offset:32768
	ds_read_b128 v[188:191], v153 offset:33792
	ds_read_b128 v[192:195], v153 offset:34816
	ds_read_b128 v[196:199], v153 offset:35840
	ds_read_b128 v[200:203], v153 offset:36864
	ds_read_b128 v[204:207], v153 offset:37888
	ds_read_b128 v[208:211], v153 offset:38912
	ds_read_b128 v[212:215], v153 offset:39936
	global_load_lds_dwordx4 v[224:225], off
	v_lshl_add_u64 v[224:225], s[26:27], 0, v[134:135]
	s_mov_b32 m0, s68
	s_nop 0
	global_load_lds_dwordx4 v[224:225], off
	s_waitcnt vmcnt(8)
	s_waitcnt lgkmcnt(0)
	s_barrier
	v_mfma_f32_16x16x32_bf16 v[126:129], v[144:147], v[184:187], v[126:129]
	v_mfma_f32_16x16x32_bf16 v[118:121], v[160:163], v[184:187], v[118:121]
	v_mfma_f32_16x16x32_bf16 v[110:113], v[144:147], v[192:195], v[110:113]
	v_mfma_f32_16x16x32_bf16 v[102:105], v[160:163], v[192:195], v[102:105]
	v_mfma_f32_16x16x32_bf16 v[94:97], v[144:147], v[200:203], v[94:97]
	v_mfma_f32_16x16x32_bf16 v[86:89], v[160:163], v[200:203], v[86:89]
	v_mfma_f32_16x16x32_bf16 v[78:81], v[144:147], v[208:211], v[78:81]
	v_mfma_f32_16x16x32_bf16 v[70:73], v[160:163], v[208:211], v[70:73]
	v_mfma_f32_16x16x32_bf16 v[126:129], v[156:159], v[188:191], v[126:129]
	v_mfma_f32_16x16x32_bf16 v[118:121], v[164:167], v[188:191], v[118:121]
	v_mfma_f32_16x16x32_bf16 v[110:113], v[156:159], v[196:199], v[110:113]
	v_mfma_f32_16x16x32_bf16 v[102:105], v[164:167], v[196:199], v[102:105]
	v_mfma_f32_16x16x32_bf16 v[94:97], v[156:159], v[204:207], v[94:97]
	v_mfma_f32_16x16x32_bf16 v[86:89], v[164:167], v[204:207], v[86:89]
	v_mfma_f32_16x16x32_bf16 v[78:81], v[156:159], v[212:215], v[78:81]
	v_mfma_f32_16x16x32_bf16 v[70:73], v[164:167], v[212:215], v[70:73]
	v_mfma_f32_16x16x32_bf16 v[122:125], v[168:171], v[184:187], v[122:125]
	v_mfma_f32_16x16x32_bf16 v[114:117], v[176:179], v[184:187], v[114:117]
	v_mfma_f32_16x16x32_bf16 v[106:109], v[168:171], v[192:195], v[106:109]
	v_mfma_f32_16x16x32_bf16 v[98:101], v[176:179], v[192:195], v[98:101]
	v_mfma_f32_16x16x32_bf16 v[90:93], v[168:171], v[200:203], v[90:93]
	v_mfma_f32_16x16x32_bf16 v[82:85], v[176:179], v[200:203], v[82:85]
	v_mfma_f32_16x16x32_bf16 v[74:77], v[168:171], v[208:211], v[74:77]
	v_mfma_f32_16x16x32_bf16 v[66:69], v[176:179], v[208:211], v[66:69]
	v_mfma_f32_16x16x32_bf16 v[122:125], v[172:175], v[188:191], v[122:125]
	v_mfma_f32_16x16x32_bf16 v[114:117], v[180:183], v[188:191], v[114:117]
	v_mfma_f32_16x16x32_bf16 v[106:109], v[172:175], v[196:199], v[106:109]
	v_mfma_f32_16x16x32_bf16 v[98:101], v[180:183], v[196:199], v[98:101]
	v_mfma_f32_16x16x32_bf16 v[90:93], v[172:175], v[204:207], v[90:93]
	v_mfma_f32_16x16x32_bf16 v[82:85], v[180:183], v[204:207], v[82:85]
	v_mfma_f32_16x16x32_bf16 v[74:77], v[172:175], v[212:215], v[74:77]
	v_mfma_f32_16x16x32_bf16 v[66:69], v[180:183], v[212:215], v[66:69]
	s_barrier
	s_add_i32 s26, s86, s35
	v_lshl_add_u64 v[224:225], v[216:217], 0, s[16:17]
	s_mov_b32 m0, s26
	ds_read_b128 v[184:187], v153 offset:49152
	ds_read_b128 v[188:191], v153 offset:50176
	ds_read_b128 v[192:195], v153 offset:51200
	ds_read_b128 v[196:199], v153 offset:52224
	ds_read_b128 v[200:203], v153 offset:53248
	ds_read_b128 v[204:207], v153 offset:54272
	ds_read_b128 v[208:211], v153 offset:55296
	ds_read_b128 v[212:215], v153 offset:56320
	global_load_lds_dwordx4 v[224:225], off
	v_lshl_add_u64 v[224:225], v[216:217], 0, s[18:19]
	s_add_i32 m0, s26, 0x2000
	s_add_i32 s26, s87, s35
	global_load_lds_dwordx4 v[224:225], off
	v_lshl_add_u64 v[224:225], v[216:217], 0, s[22:23]
	s_mov_b32 m0, s26
	v_lshl_add_u64 v[216:217], v[216:217], 0, s[24:25]
	global_load_lds_dwordx4 v[224:225], off
	s_add_i32 m0, s26, 0x2000
	s_nop 0
	global_load_lds_dwordx4 v[216:217], off
	v_lshl_add_u64 v[216:217], v[220:221], 0, s[20:21]
	s_mov_b32 m0, s70
	s_nop 0
	global_load_lds_dwordx4 v[216:217], off
	v_lshl_add_u64 v[216:217], v[222:223], 0, s[20:21]
	s_mov_b32 m0, s71
	s_nop 0
	global_load_lds_dwordx4 v[216:217], off
	s_waitcnt vmcnt(8)
	s_waitcnt lgkmcnt(0)
	s_barrier
	v_mfma_f32_16x16x32_bf16 v[62:65], v[144:147], v[184:187], v[62:65]
	v_mfma_f32_16x16x32_bf16 v[54:57], v[160:163], v[184:187], v[54:57]
	v_mfma_f32_16x16x32_bf16 v[46:49], v[144:147], v[192:195], v[46:49]
	v_mfma_f32_16x16x32_bf16 v[38:41], v[160:163], v[192:195], v[38:41]
	v_mfma_f32_16x16x32_bf16 v[30:33], v[144:147], v[200:203], v[30:33]
	v_mfma_f32_16x16x32_bf16 v[22:25], v[160:163], v[200:203], v[22:25]
	v_mfma_f32_16x16x32_bf16 v[14:17], v[144:147], v[208:211], v[14:17]
	v_mfma_f32_16x16x32_bf16 v[6:9], v[160:163], v[208:211], v[6:9]
	v_mfma_f32_16x16x32_bf16 v[62:65], v[156:159], v[188:191], v[62:65]
	v_mfma_f32_16x16x32_bf16 v[54:57], v[164:167], v[188:191], v[54:57]
	v_mfma_f32_16x16x32_bf16 v[46:49], v[156:159], v[196:199], v[46:49]
	v_mfma_f32_16x16x32_bf16 v[38:41], v[164:167], v[196:199], v[38:41]
	v_mfma_f32_16x16x32_bf16 v[30:33], v[156:159], v[204:207], v[30:33]
	v_mfma_f32_16x16x32_bf16 v[22:25], v[164:167], v[204:207], v[22:25]
	v_mfma_f32_16x16x32_bf16 v[14:17], v[156:159], v[212:215], v[14:17]
	v_mfma_f32_16x16x32_bf16 v[6:9], v[164:167], v[212:215], v[6:9]
	v_mfma_f32_16x16x32_bf16 v[58:61], v[168:171], v[184:187], v[58:61]
	v_mfma_f32_16x16x32_bf16 v[50:53], v[176:179], v[184:187], v[50:53]
	v_mfma_f32_16x16x32_bf16 v[42:45], v[168:171], v[192:195], v[42:45]
	v_mfma_f32_16x16x32_bf16 v[34:37], v[176:179], v[192:195], v[34:37]
	v_mfma_f32_16x16x32_bf16 v[26:29], v[168:171], v[200:203], v[26:29]
	v_mfma_f32_16x16x32_bf16 v[18:21], v[176:179], v[200:203], v[18:21]
	v_mfma_f32_16x16x32_bf16 v[10:13], v[168:171], v[208:211], v[10:13]
	v_mfma_f32_16x16x32_bf16 v[2:5], v[176:179], v[208:211], v[2:5]
	v_mfma_f32_16x16x32_bf16 v[58:61], v[172:175], v[188:191], v[58:61]
	v_mfma_f32_16x16x32_bf16 v[50:53], v[180:183], v[188:191], v[50:53]
	v_mfma_f32_16x16x32_bf16 v[42:45], v[172:175], v[196:199], v[42:45]
	v_mfma_f32_16x16x32_bf16 v[34:37], v[180:183], v[196:199], v[34:37]
	v_mfma_f32_16x16x32_bf16 v[26:29], v[172:175], v[204:207], v[26:29]
	v_mfma_f32_16x16x32_bf16 v[18:21], v[180:183], v[204:207], v[18:21]
	v_mfma_f32_16x16x32_bf16 v[10:13], v[172:175], v[212:215], v[10:13]
	v_mfma_f32_16x16x32_bf16 v[2:5], v[180:183], v[212:215], v[2:5]
	s_barrier
	s_add_i32 s85, s85, 2
	s_add_u32 s83, s83, 0x10000
	s_addc_u32 s84, s84, 0
	s_add_u32 s62, s62, 0x100
	s_addc_u32 s63, s63, 0
	s_cmp_gt_u32 s85, 29
	s_cbranch_scc0 .LBB0_783
	s_and_b64 vcc, exec, s[40:41]
	s_cbranch_vccz .LBB0_786
	s_barrier

.LBB0_858:
	ds_read_b128 v[26:29], v185
	ds_read_b128 v[30:33], v185 offset:1024
	ds_read_b128 v[18:21], v185 offset:2048
	ds_read_b128 v[22:25], v185 offset:3072
	ds_read_b128 v[10:13], v186
	ds_read_b128 v[14:17], v186 offset:1024
	ds_read_b128 v[2:5], v186 offset:2048
	ds_read_b128 v[6:9], v186 offset:3072
	s_add_u32 s26, s50, 0xfff50080
	s_addc_u32 s27, s51, -1
	s_cmp_eq_u32 s74, 40
	s_cselect_b32 s53, s5, s27
	s_cselect_b32 s52, s4, s26
	s_cselect_b32 s55, s45, s73
	s_cselect_b32 s54, s44, s72
	v_lshl_add_u64 v[176:177], s[50:51], 0, v[168:169]
	s_add_i32 m0, s59, 0xc000
	ds_read_b128 v[190:193], v187
	ds_read_b128 v[194:197], v187 offset:1024
	ds_read_b128 v[198:201], v187 offset:2048
	ds_read_b128 v[202:205], v187 offset:3072
	ds_read_b128 v[206:209], v187 offset:4096
	ds_read_b128 v[210:213], v187 offset:5120
	ds_read_b128 v[220:223], v187 offset:6144
	ds_read_b128 v[224:227], v187 offset:7168
	global_load_lds_dwordx4 v[176:177], off
	v_lshl_add_u64 v[176:177], s[50:51], 0, v[170:171]
	s_add_i32 m0, s59, 0xe000
	s_nop 0
	global_load_lds_dwordx4 v[176:177], off
	s_waitcnt vmcnt(8)
	s_waitcnt lgkmcnt(0)
	s_barrier
	v_mfma_scale_f32_16x16x128_f8f6f4 v[158:161], v[26:33], v[190:197], v[158:161], v188, v189 op_sel_hi:[0,0,0]
	v_mfma_scale_f32_16x16x128_f8f6f4 v[154:157], v[18:25], v[190:197], v[154:157], v188, v189 op_sel_hi:[0,0,0]
	v_mfma_scale_f32_16x16x128_f8f6f4 v[150:153], v[26:33], v[198:205], v[150:153], v188, v189 op_sel_hi:[0,0,0]
	v_mfma_scale_f32_16x16x128_f8f6f4 v[146:149], v[18:25], v[198:205], v[146:149], v188, v189 op_sel_hi:[0,0,0]
	v_mfma_scale_f32_16x16x128_f8f6f4 v[138:141], v[26:33], v[206:213], v[138:141], v188, v189 op_sel_hi:[0,0,0]
	v_mfma_scale_f32_16x16x128_f8f6f4 v[130:133], v[18:25], v[206:213], v[130:133], v188, v189 op_sel_hi:[0,0,0]
	v_mfma_scale_f32_16x16x128_f8f6f4 v[122:125], v[26:33], v[220:227], v[122:125], v188, v189 op_sel_hi:[0,0,0]
	v_mfma_scale_f32_16x16x128_f8f6f4 v[114:117], v[18:25], v[220:227], v[114:117], v188, v189 op_sel_hi:[0,0,0]
	v_mfma_scale_f32_16x16x128_f8f6f4 v[142:145], v[10:17], v[190:197], v[142:145], v188, v189 op_sel_hi:[0,0,0]
	v_mfma_scale_f32_16x16x128_f8f6f4 v[134:137], v[2:9], v[190:197], v[134:137], v188, v189 op_sel_hi:[0,0,0]
	v_mfma_scale_f32_16x16x128_f8f6f4 v[126:129], v[10:17], v[198:205], v[126:129], v188, v189 op_sel_hi:[0,0,0]
	v_mfma_scale_f32_16x16x128_f8f6f4 v[118:121], v[2:9], v[198:205], v[118:121], v188, v189 op_sel_hi:[0,0,0]
	v_mfma_scale_f32_16x16x128_f8f6f4 v[110:113], v[10:17], v[206:213], v[110:113], v188, v189 op_sel_hi:[0,0,0]
	v_mfma_scale_f32_16x16x128_f8f6f4 v[106:109], v[2:9], v[206:213], v[106:109], v188, v189 op_sel_hi:[0,0,0]
	v_mfma_scale_f32_16x16x128_f8f6f4 v[102:105], v[10:17], v[220:227], v[102:105], v188, v189 op_sel_hi:[0,0,0]
	v_mfma_scale_f32_16x16x128_f8f6f4 v[98:101], v[2:9], v[220:227], v[98:101], v188, v189 op_sel_hi:[0,0,0]
	s_barrier
	s_add_i32 s26, s67, s57
	v_lshl_add_u64 v[176:177], s[54:55], 0, v[162:163]
	s_mov_b32 m0, s26
	ds_read_b128 v[190:193], v187 offset:16384
	ds_read_b128 v[194:197], v187 offset:17408
	ds_read_b128 v[198:201], v187 offset:18432
	ds_read_b128 v[202:205], v187 offset:19456
	ds_read_b128 v[206:209], v187 offset:20480
	ds_read_b128 v[210:213], v187 offset:21504
	ds_read_b128 v[220:223], v187 offset:22528
	ds_read_b128 v[224:227], v187 offset:23552
	global_load_lds_dwordx4 v[176:177], off
	v_lshl_add_u64 v[178:179], v[176:177], 0, s[8:9]
	s_add_i32 m0, s26, 0x2000
	s_add_i32 s26, s68, s57
	global_load_lds_dwordx4 v[178:179], off
	v_lshl_add_u64 v[178:179], v[176:177], 0, s[10:11]
	s_mov_b32 m0, s26
	v_lshl_add_u64 v[180:181], s[52:53], 0, v[166:167]
	global_load_lds_dwordx4 v[178:179], off
	v_lshl_add_u64 v[178:179], v[176:177], 0, s[12:13]
	s_add_i32 m0, s26, 0x2000
	s_nop 0
	global_load_lds_dwordx4 v[178:179], off
	v_lshl_add_u64 v[178:179], s[52:53], 0, v[164:165]
	s_mov_b32 m0, s59
	s_nop 0
	global_load_lds_dwordx4 v[178:179], off
	s_mov_b32 m0, s60
	s_nop 0
	global_load_lds_dwordx4 v[180:181], off
	s_waitcnt vmcnt(8)
	s_waitcnt lgkmcnt(0)
	s_barrier
	v_mfma_scale_f32_16x16x128_f8f6f4 v[94:97], v[26:33], v[190:197], v[94:97], v188, v189 op_sel_hi:[0,0,0]
	v_mfma_scale_f32_16x16x128_f8f6f4 v[90:93], v[18:25], v[190:197], v[90:93], v188, v189 op_sel_hi:[0,0,0]
	v_mfma_scale_f32_16x16x128_f8f6f4 v[86:89], v[26:33], v[198:205], v[86:89], v188, v189 op_sel_hi:[0,0,0]
	v_mfma_scale_f32_16x16x128_f8f6f4 v[78:81], v[18:25], v[198:205], v[78:81], v188, v189 op_sel_hi:[0,0,0]
	v_mfma_scale_f32_16x16x128_f8f6f4 v[70:73], v[26:33], v[206:213], v[70:73], v188, v189 op_sel_hi:[0,0,0]
	v_mfma_scale_f32_16x16x128_f8f6f4 v[62:65], v[18:25], v[206:213], v[62:65], v188, v189 op_sel_hi:[0,0,0]
	v_mfma_scale_f32_16x16x128_f8f6f4 v[54:57], v[26:33], v[220:227], v[54:57], v188, v189 op_sel_hi:[0,0,0]
	v_mfma_scale_f32_16x16x128_f8f6f4 v[46:49], v[18:25], v[220:227], v[46:49], v188, v189 op_sel_hi:[0,0,0]
	v_mfma_scale_f32_16x16x128_f8f6f4 v[82:85], v[10:17], v[190:197], v[82:85], v188, v189 op_sel_hi:[0,0,0]
	v_mfma_scale_f32_16x16x128_f8f6f4 v[74:77], v[2:9], v[190:197], v[74:77], v188, v189 op_sel_hi:[0,0,0]
	v_mfma_scale_f32_16x16x128_f8f6f4 v[66:69], v[10:17], v[198:205], v[66:69], v188, v189 op_sel_hi:[0,0,0]
	v_mfma_scale_f32_16x16x128_f8f6f4 v[58:61], v[2:9], v[198:205], v[58:61], v188, v189 op_sel_hi:[0,0,0]
	v_mfma_scale_f32_16x16x128_f8f6f4 v[50:53], v[10:17], v[206:213], v[50:53], v188, v189 op_sel_hi:[0,0,0]
	v_mfma_scale_f32_16x16x128_f8f6f4 v[42:45], v[2:9], v[206:213], v[42:45], v188, v189 op_sel_hi:[0,0,0]
	v_mfma_scale_f32_16x16x128_f8f6f4 v[38:41], v[10:17], v[220:227], v[38:41], v188, v189 op_sel_hi:[0,0,0]
	v_mfma_scale_f32_16x16x128_f8f6f4 v[34:37], v[2:9], v[220:227], v[34:37], v188, v189 op_sel_hi:[0,0,0]
	s_barrier
	s_add_i32 s54, 0, 0x18000
	s_add_i32 s55, 0, 0x1c000
	v_add_u32_e32 v14, s54, v183
	v_add_u32_e32 v30, s55, v183
	ds_read_b128 v[2:5], v14
	ds_read_b128 v[6:9], v14 offset:1024
	ds_read_b128 v[10:13], v14 offset:2048
	ds_read_b128 v[14:17], v14 offset:3072
	ds_read_b128 v[18:21], v30
	ds_read_b128 v[22:25], v30 offset:1024
	ds_read_b128 v[26:29], v30 offset:2048
	ds_read_b128 v[30:33], v30 offset:3072
	s_add_u32 s26, s52, 0xb0000
	s_addc_u32 s27, s53, 0
	s_mov_b32 m0, s61
	v_lshl_add_u64 v[214:215], s[26:27], 0, v[164:165]
	ds_read_b128 v[190:193], v187 offset:32768
	ds_read_b128 v[194:197], v187 offset:33792
	ds_read_b128 v[198:201], v187 offset:34816
	ds_read_b128 v[202:205], v187 offset:35840
	ds_read_b128 v[206:209], v187 offset:36864
	ds_read_b128 v[210:213], v187 offset:37888
	ds_read_b128 v[220:223], v187 offset:38912
	ds_read_b128 v[224:227], v187 offset:39936
	global_load_lds_dwordx4 v[214:215], off
	v_lshl_add_u64 v[214:215], s[26:27], 0, v[166:167]
	s_mov_b32 m0, s62
	s_nop 0
	global_load_lds_dwordx4 v[214:215], off
	s_waitcnt vmcnt(8)
	s_waitcnt lgkmcnt(0)
	s_barrier
	v_mfma_scale_f32_16x16x128_f8f6f4 v[158:161], v[2:9], v[190:197], v[158:161], v188, v189 op_sel_hi:[0,0,0]
	v_mfma_scale_f32_16x16x128_f8f6f4 v[154:157], v[10:17], v[190:197], v[154:157], v188, v189 op_sel_hi:[0,0,0]
	v_mfma_scale_f32_16x16x128_f8f6f4 v[150:153], v[2:9], v[198:205], v[150:153], v188, v189 op_sel_hi:[0,0,0]
	v_mfma_scale_f32_16x16x128_f8f6f4 v[146:149], v[10:17], v[198:205], v[146:149], v188, v189 op_sel_hi:[0,0,0]
	v_mfma_scale_f32_16x16x128_f8f6f4 v[138:141], v[2:9], v[206:213], v[138:141], v188, v189 op_sel_hi:[0,0,0]
	v_mfma_scale_f32_16x16x128_f8f6f4 v[130:133], v[10:17], v[206:213], v[130:133], v188, v189 op_sel_hi:[0,0,0]
	v_mfma_scale_f32_16x16x128_f8f6f4 v[122:125], v[2:9], v[220:227], v[122:125], v188, v189 op_sel_hi:[0,0,0]
	v_mfma_scale_f32_16x16x128_f8f6f4 v[114:117], v[10:17], v[220:227], v[114:117], v188, v189 op_sel_hi:[0,0,0]
	v_mfma_scale_f32_16x16x128_f8f6f4 v[142:145], v[18:25], v[190:197], v[142:145], v188, v189 op_sel_hi:[0,0,0]
	v_mfma_scale_f32_16x16x128_f8f6f4 v[134:137], v[26:33], v[190:197], v[134:137], v188, v189 op_sel_hi:[0,0,0]
	v_mfma_scale_f32_16x16x128_f8f6f4 v[126:129], v[18:25], v[198:205], v[126:129], v188, v189 op_sel_hi:[0,0,0]
	v_mfma_scale_f32_16x16x128_f8f6f4 v[118:121], v[26:33], v[198:205], v[118:121], v188, v189 op_sel_hi:[0,0,0]
	v_mfma_scale_f32_16x16x128_f8f6f4 v[110:113], v[18:25], v[206:213], v[110:113], v188, v189 op_sel_hi:[0,0,0]
	v_mfma_scale_f32_16x16x128_f8f6f4 v[106:109], v[26:33], v[206:213], v[106:109], v188, v189 op_sel_hi:[0,0,0]
	v_mfma_scale_f32_16x16x128_f8f6f4 v[102:105], v[18:25], v[220:227], v[102:105], v188, v189 op_sel_hi:[0,0,0]
	v_mfma_scale_f32_16x16x128_f8f6f4 v[98:101], v[26:33], v[220:227], v[98:101], v188, v189 op_sel_hi:[0,0,0]
	s_barrier
	s_add_i32 s26, s54, s57
	v_lshl_add_u64 v[214:215], v[176:177], 0, s[16:17]
	s_mov_b32 m0, s26
	ds_read_b128 v[190:193], v187 offset:49152
	ds_read_b128 v[194:197], v187 offset:50176
	ds_read_b128 v[198:201], v187 offset:51200
	ds_read_b128 v[202:205], v187 offset:52224
	ds_read_b128 v[206:209], v187 offset:53248
	ds_read_b128 v[210:213], v187 offset:54272
	ds_read_b128 v[220:223], v187 offset:55296
	ds_read_b128 v[224:227], v187 offset:56320
	global_load_lds_dwordx4 v[214:215], off
	v_lshl_add_u64 v[214:215], v[176:177], 0, s[18:19]
	s_add_i32 m0, s26, 0x2000
	s_add_i32 s26, s55, s57
	global_load_lds_dwordx4 v[214:215], off
	v_lshl_add_u64 v[214:215], v[176:177], 0, s[22:23]
	s_mov_b32 m0, s26
	v_lshl_add_u64 v[176:177], v[176:177], 0, s[24:25]
	global_load_lds_dwordx4 v[214:215], off
	s_add_i32 m0, s26, 0x2000
	s_nop 0
	global_load_lds_dwordx4 v[176:177], off
	v_lshl_add_u64 v[176:177], v[178:179], 0, s[20:21]
	s_mov_b32 m0, s64
	s_nop 0
	global_load_lds_dwordx4 v[176:177], off
	v_lshl_add_u64 v[176:177], v[180:181], 0, s[20:21]
	s_mov_b32 m0, s65
	s_nop 0
	global_load_lds_dwordx4 v[176:177], off
	s_waitcnt vmcnt(8)
	s_waitcnt lgkmcnt(0)
	s_barrier
	v_mfma_scale_f32_16x16x128_f8f6f4 v[94:97], v[2:9], v[190:197], v[94:97], v188, v189 op_sel_hi:[0,0,0]
	v_mfma_scale_f32_16x16x128_f8f6f4 v[90:93], v[10:17], v[190:197], v[90:93], v188, v189 op_sel_hi:[0,0,0]
	v_mfma_scale_f32_16x16x128_f8f6f4 v[86:89], v[2:9], v[198:205], v[86:89], v188, v189 op_sel_hi:[0,0,0]
	v_mfma_scale_f32_16x16x128_f8f6f4 v[78:81], v[10:17], v[198:205], v[78:81], v188, v189 op_sel_hi:[0,0,0]
	v_mfma_scale_f32_16x16x128_f8f6f4 v[70:73], v[2:9], v[206:213], v[70:73], v188, v189 op_sel_hi:[0,0,0]
	v_mfma_scale_f32_16x16x128_f8f6f4 v[62:65], v[10:17], v[206:213], v[62:65], v188, v189 op_sel_hi:[0,0,0]
	v_mfma_scale_f32_16x16x128_f8f6f4 v[54:57], v[2:9], v[220:227], v[54:57], v188, v189 op_sel_hi:[0,0,0]
	v_mfma_scale_f32_16x16x128_f8f6f4 v[46:49], v[10:17], v[220:227], v[46:49], v188, v189 op_sel_hi:[0,0,0]
	v_mfma_scale_f32_16x16x128_f8f6f4 v[82:85], v[18:25], v[190:197], v[82:85], v188, v189 op_sel_hi:[0,0,0]
	v_mfma_scale_f32_16x16x128_f8f6f4 v[74:77], v[26:33], v[190:197], v[74:77], v188, v189 op_sel_hi:[0,0,0]
	v_mfma_scale_f32_16x16x128_f8f6f4 v[66:69], v[18:25], v[198:205], v[66:69], v188, v189 op_sel_hi:[0,0,0]
	v_mfma_scale_f32_16x16x128_f8f6f4 v[58:61], v[26:33], v[198:205], v[58:61], v188, v189 op_sel_hi:[0,0,0]
	v_mfma_scale_f32_16x16x128_f8f6f4 v[50:53], v[18:25], v[206:213], v[50:53], v188, v189 op_sel_hi:[0,0,0]
	v_mfma_scale_f32_16x16x128_f8f6f4 v[42:45], v[26:33], v[206:213], v[42:45], v188, v189 op_sel_hi:[0,0,0]
	v_mfma_scale_f32_16x16x128_f8f6f4 v[38:41], v[18:25], v[220:227], v[38:41], v188, v189 op_sel_hi:[0,0,0]
	v_mfma_scale_f32_16x16x128_f8f6f4 v[34:37], v[26:33], v[220:227], v[34:37], v188, v189 op_sel_hi:[0,0,0]
	s_barrier
	s_add_i32 s74, s74, 2
	s_add_u32 s72, s72, 0x10000
	s_addc_u32 s73, s73, 0
	s_add_u32 s50, s50, 0x100
	s_addc_u32 s51, s51, 0
	s_cmp_gt_u32 s74, 41
	s_cbranch_scc0 .LBB0_858
	s_and_b64 vcc, exec, s[40:41]
	s_cbranch_vccz .LBB0_861
	s_barrier

.LBB0_985:
	ds_read_b128 v[26:29], v185
	ds_read_b128 v[30:33], v185 offset:1024
	ds_read_b128 v[18:21], v185 offset:2048
	ds_read_b128 v[22:25], v185 offset:3072
	ds_read_b128 v[10:13], v186
	ds_read_b128 v[14:17], v186 offset:1024
	ds_read_b128 v[2:5], v186 offset:2048
	ds_read_b128 v[6:9], v186 offset:3072
	s_add_u32 s26, s56, 0xfffc0080
	s_addc_u32 s27, s57, -1
	s_cmp_eq_u32 s80, 12
	s_cselect_b32 s59, s45, s27
	s_cselect_b32 s58, s72, s26
	s_cselect_b32 s61, s41, s75
	s_cselect_b32 s60, s73, s74
	v_lshl_add_u64 v[176:177], s[56:57], 0, v[168:169]
	s_add_i32 m0, s55, 0xc000
	ds_read_b128 v[192:195], v187
	ds_read_b128 v[196:199], v187 offset:1024
	ds_read_b128 v[200:203], v187 offset:2048
	ds_read_b128 v[204:207], v187 offset:3072
	ds_read_b128 v[208:211], v187 offset:4096
	ds_read_b128 v[212:215], v187 offset:5120
	ds_read_b128 v[220:223], v187 offset:6144
	ds_read_b128 v[224:227], v187 offset:7168
	global_load_lds_dwordx4 v[176:177], off
	v_lshl_add_u64 v[176:177], s[56:57], 0, v[170:171]
	s_add_i32 m0, s55, 0xe000
	s_nop 0
	global_load_lds_dwordx4 v[176:177], off
	s_waitcnt vmcnt(8)
	s_waitcnt lgkmcnt(0)
	s_barrier
	v_mfma_scale_f32_16x16x128_f8f6f4 v[158:161], v[26:33], v[192:199], v[158:161], v188, v189 op_sel_hi:[0,0,0]
	v_mfma_scale_f32_16x16x128_f8f6f4 v[154:157], v[18:25], v[192:199], v[154:157], v188, v189 op_sel_hi:[0,0,0]
	v_mfma_scale_f32_16x16x128_f8f6f4 v[146:149], v[26:33], v[200:207], v[146:149], v188, v189 op_sel_hi:[0,0,0]
	v_mfma_scale_f32_16x16x128_f8f6f4 v[138:141], v[18:25], v[200:207], v[138:141], v188, v189 op_sel_hi:[0,0,0]
	v_mfma_scale_f32_16x16x128_f8f6f4 v[130:133], v[26:33], v[208:215], v[130:133], v188, v189 op_sel_hi:[0,0,0]
	v_mfma_scale_f32_16x16x128_f8f6f4 v[122:125], v[18:25], v[208:215], v[122:125], v188, v189 op_sel_hi:[0,0,0]
	v_mfma_scale_f32_16x16x128_f8f6f4 v[114:117], v[26:33], v[220:227], v[114:117], v188, v189 op_sel_hi:[0,0,0]
	v_mfma_scale_f32_16x16x128_f8f6f4 v[106:109], v[18:25], v[220:227], v[106:109], v188, v189 op_sel_hi:[0,0,0]
	v_mfma_scale_f32_16x16x128_f8f6f4 v[150:153], v[10:17], v[192:199], v[150:153], v188, v189 op_sel_hi:[0,0,0]
	v_mfma_scale_f32_16x16x128_f8f6f4 v[142:145], v[2:9], v[192:199], v[142:145], v188, v189 op_sel_hi:[0,0,0]
	v_mfma_scale_f32_16x16x128_f8f6f4 v[134:137], v[10:17], v[200:207], v[134:137], v188, v189 op_sel_hi:[0,0,0]
	v_mfma_scale_f32_16x16x128_f8f6f4 v[126:129], v[2:9], v[200:207], v[126:129], v188, v189 op_sel_hi:[0,0,0]
	v_mfma_scale_f32_16x16x128_f8f6f4 v[118:121], v[10:17], v[208:215], v[118:121], v188, v189 op_sel_hi:[0,0,0]
	v_mfma_scale_f32_16x16x128_f8f6f4 v[110:113], v[2:9], v[208:215], v[110:113], v188, v189 op_sel_hi:[0,0,0]
	v_mfma_scale_f32_16x16x128_f8f6f4 v[102:105], v[10:17], v[220:227], v[102:105], v188, v189 op_sel_hi:[0,0,0]
	v_mfma_scale_f32_16x16x128_f8f6f4 v[98:101], v[2:9], v[220:227], v[98:101], v188, v189 op_sel_hi:[0,0,0]
	s_barrier
	s_add_i32 s26, s70, s35
	v_lshl_add_u64 v[176:177], s[60:61], 0, v[162:163]
	s_mov_b32 m0, s26
	ds_read_b128 v[192:195], v187 offset:16384
	ds_read_b128 v[196:199], v187 offset:17408
	ds_read_b128 v[200:203], v187 offset:18432
	ds_read_b128 v[204:207], v187 offset:19456
	ds_read_b128 v[208:211], v187 offset:20480
	ds_read_b128 v[212:215], v187 offset:21504
	ds_read_b128 v[220:223], v187 offset:22528
	ds_read_b128 v[224:227], v187 offset:23552
	global_load_lds_dwordx4 v[176:177], off
	v_lshl_add_u64 v[178:179], v[176:177], 0, s[6:7]
	s_add_i32 m0, s26, 0x2000
	s_add_i32 s26, s71, s35
	global_load_lds_dwordx4 v[178:179], off
	v_lshl_add_u64 v[178:179], v[176:177], 0, s[8:9]
	s_mov_b32 m0, s26
	v_lshl_add_u64 v[180:181], s[58:59], 0, v[166:167]
	global_load_lds_dwordx4 v[178:179], off
	v_lshl_add_u64 v[178:179], v[176:177], 0, s[10:11]
	s_add_i32 m0, s26, 0x2000
	s_nop 0
	global_load_lds_dwordx4 v[178:179], off
	v_lshl_add_u64 v[178:179], s[58:59], 0, v[164:165]
	s_mov_b32 m0, s55
	s_nop 0
	global_load_lds_dwordx4 v[178:179], off
	s_mov_b32 m0, s63
	s_nop 0
	global_load_lds_dwordx4 v[180:181], off
	s_waitcnt vmcnt(8)
	s_waitcnt lgkmcnt(0)
	s_barrier
	v_mfma_scale_f32_16x16x128_f8f6f4 v[94:97], v[26:33], v[192:199], v[94:97], v188, v189 op_sel_hi:[0,0,0]
	v_mfma_scale_f32_16x16x128_f8f6f4 v[90:93], v[18:25], v[192:199], v[90:93], v188, v189 op_sel_hi:[0,0,0]
	v_mfma_scale_f32_16x16x128_f8f6f4 v[82:85], v[26:33], v[200:207], v[82:85], v188, v189 op_sel_hi:[0,0,0]
	v_mfma_scale_f32_16x16x128_f8f6f4 v[74:77], v[18:25], v[200:207], v[74:77], v188, v189 op_sel_hi:[0,0,0]
	v_mfma_scale_f32_16x16x128_f8f6f4 v[66:69], v[26:33], v[208:215], v[66:69], v188, v189 op_sel_hi:[0,0,0]
	v_mfma_scale_f32_16x16x128_f8f6f4 v[58:61], v[18:25], v[208:215], v[58:61], v188, v189 op_sel_hi:[0,0,0]
	v_mfma_scale_f32_16x16x128_f8f6f4 v[50:53], v[26:33], v[220:227], v[50:53], v188, v189 op_sel_hi:[0,0,0]
	v_mfma_scale_f32_16x16x128_f8f6f4 v[42:45], v[18:25], v[220:227], v[42:45], v188, v189 op_sel_hi:[0,0,0]
	v_mfma_scale_f32_16x16x128_f8f6f4 v[86:89], v[10:17], v[192:199], v[86:89], v188, v189 op_sel_hi:[0,0,0]
	v_mfma_scale_f32_16x16x128_f8f6f4 v[78:81], v[2:9], v[192:199], v[78:81], v188, v189 op_sel_hi:[0,0,0]
	v_mfma_scale_f32_16x16x128_f8f6f4 v[70:73], v[10:17], v[200:207], v[70:73], v188, v189 op_sel_hi:[0,0,0]
	v_mfma_scale_f32_16x16x128_f8f6f4 v[62:65], v[2:9], v[200:207], v[62:65], v188, v189 op_sel_hi:[0,0,0]
	v_mfma_scale_f32_16x16x128_f8f6f4 v[54:57], v[10:17], v[208:215], v[54:57], v188, v189 op_sel_hi:[0,0,0]
	v_mfma_scale_f32_16x16x128_f8f6f4 v[46:49], v[2:9], v[208:215], v[46:49], v188, v189 op_sel_hi:[0,0,0]
	v_mfma_scale_f32_16x16x128_f8f6f4 v[38:41], v[10:17], v[220:227], v[38:41], v188, v189 op_sel_hi:[0,0,0]
	v_mfma_scale_f32_16x16x128_f8f6f4 v[34:37], v[2:9], v[220:227], v[34:37], v188, v189 op_sel_hi:[0,0,0]
	s_barrier
	s_add_i32 s60, 0, 0x18000
	s_add_i32 s61, 0, 0x1c000
	v_add_u32_e32 v14, s60, v183
	v_add_u32_e32 v30, s61, v183
	ds_read_b128 v[2:5], v14
	ds_read_b128 v[6:9], v14 offset:1024
	ds_read_b128 v[10:13], v14 offset:2048
	ds_read_b128 v[14:17], v14 offset:3072
	ds_read_b128 v[18:21], v30
	ds_read_b128 v[22:25], v30 offset:1024
	ds_read_b128 v[26:29], v30 offset:2048
	ds_read_b128 v[30:33], v30 offset:3072
	s_add_u32 s26, s58, 0x40000
	s_addc_u32 s27, s59, 0
	s_mov_b32 m0, s64
	v_lshl_add_u64 v[216:217], s[26:27], 0, v[164:165]
	ds_read_b128 v[192:195], v187 offset:32768
	ds_read_b128 v[196:199], v187 offset:33792
	ds_read_b128 v[200:203], v187 offset:34816
	ds_read_b128 v[204:207], v187 offset:35840
	ds_read_b128 v[208:211], v187 offset:36864
	ds_read_b128 v[212:215], v187 offset:37888
	ds_read_b128 v[220:223], v187 offset:38912
	ds_read_b128 v[224:227], v187 offset:39936
	global_load_lds_dwordx4 v[216:217], off
	v_lshl_add_u64 v[216:217], s[26:27], 0, v[166:167]
	s_mov_b32 m0, s65
	s_nop 0
	global_load_lds_dwordx4 v[216:217], off
	s_waitcnt vmcnt(8)
	s_waitcnt lgkmcnt(0)
	s_barrier
	v_mfma_scale_f32_16x16x128_f8f6f4 v[158:161], v[2:9], v[192:199], v[158:161], v188, v189 op_sel_hi:[0,0,0]
	v_mfma_scale_f32_16x16x128_f8f6f4 v[154:157], v[10:17], v[192:199], v[154:157], v188, v189 op_sel_hi:[0,0,0]
	v_mfma_scale_f32_16x16x128_f8f6f4 v[146:149], v[2:9], v[200:207], v[146:149], v188, v189 op_sel_hi:[0,0,0]
	v_mfma_scale_f32_16x16x128_f8f6f4 v[138:141], v[10:17], v[200:207], v[138:141], v188, v189 op_sel_hi:[0,0,0]
	v_mfma_scale_f32_16x16x128_f8f6f4 v[130:133], v[2:9], v[208:215], v[130:133], v188, v189 op_sel_hi:[0,0,0]
	v_mfma_scale_f32_16x16x128_f8f6f4 v[122:125], v[10:17], v[208:215], v[122:125], v188, v189 op_sel_hi:[0,0,0]
	v_mfma_scale_f32_16x16x128_f8f6f4 v[114:117], v[2:9], v[220:227], v[114:117], v188, v189 op_sel_hi:[0,0,0]
	v_mfma_scale_f32_16x16x128_f8f6f4 v[106:109], v[10:17], v[220:227], v[106:109], v188, v189 op_sel_hi:[0,0,0]
	v_mfma_scale_f32_16x16x128_f8f6f4 v[150:153], v[18:25], v[192:199], v[150:153], v188, v189 op_sel_hi:[0,0,0]
	v_mfma_scale_f32_16x16x128_f8f6f4 v[142:145], v[26:33], v[192:199], v[142:145], v188, v189 op_sel_hi:[0,0,0]
	v_mfma_scale_f32_16x16x128_f8f6f4 v[134:137], v[18:25], v[200:207], v[134:137], v188, v189 op_sel_hi:[0,0,0]
	v_mfma_scale_f32_16x16x128_f8f6f4 v[126:129], v[26:33], v[200:207], v[126:129], v188, v189 op_sel_hi:[0,0,0]
	v_mfma_scale_f32_16x16x128_f8f6f4 v[118:121], v[18:25], v[208:215], v[118:121], v188, v189 op_sel_hi:[0,0,0]
	v_mfma_scale_f32_16x16x128_f8f6f4 v[110:113], v[26:33], v[208:215], v[110:113], v188, v189 op_sel_hi:[0,0,0]
	v_mfma_scale_f32_16x16x128_f8f6f4 v[102:105], v[18:25], v[220:227], v[102:105], v188, v189 op_sel_hi:[0,0,0]
	v_mfma_scale_f32_16x16x128_f8f6f4 v[98:101], v[26:33], v[220:227], v[98:101], v188, v189 op_sel_hi:[0,0,0]
	s_barrier
	s_add_i32 s26, s60, s35
	v_lshl_add_u64 v[216:217], v[176:177], 0, s[14:15]
	s_mov_b32 m0, s26
	ds_read_b128 v[192:195], v187 offset:49152
	ds_read_b128 v[196:199], v187 offset:50176
	ds_read_b128 v[200:203], v187 offset:51200
	ds_read_b128 v[204:207], v187 offset:52224
	ds_read_b128 v[208:211], v187 offset:53248
	ds_read_b128 v[212:215], v187 offset:54272
	ds_read_b128 v[220:223], v187 offset:55296
	ds_read_b128 v[224:227], v187 offset:56320
	global_load_lds_dwordx4 v[216:217], off
	v_lshl_add_u64 v[216:217], v[176:177], 0, s[16:17]
	s_add_i32 m0, s26, 0x2000
	s_add_i32 s26, s61, s35
	global_load_lds_dwordx4 v[216:217], off
	v_lshl_add_u64 v[216:217], v[176:177], 0, s[20:21]
	s_mov_b32 m0, s26
	v_lshl_add_u64 v[176:177], v[176:177], 0, s[22:23]
	global_load_lds_dwordx4 v[216:217], off
	s_add_i32 m0, s26, 0x2000
	s_nop 0
	global_load_lds_dwordx4 v[176:177], off
	v_lshl_add_u64 v[176:177], v[178:179], 0, s[18:19]
	s_mov_b32 m0, s67
	s_nop 0
	global_load_lds_dwordx4 v[176:177], off
	v_lshl_add_u64 v[176:177], v[180:181], 0, s[18:19]
	s_mov_b32 m0, s68
	s_nop 0
	global_load_lds_dwordx4 v[176:177], off
	s_waitcnt vmcnt(8)
	s_waitcnt lgkmcnt(0)
	s_barrier
	v_mfma_scale_f32_16x16x128_f8f6f4 v[94:97], v[2:9], v[192:199], v[94:97], v188, v189 op_sel_hi:[0,0,0]
	v_mfma_scale_f32_16x16x128_f8f6f4 v[90:93], v[10:17], v[192:199], v[90:93], v188, v189 op_sel_hi:[0,0,0]
	v_mfma_scale_f32_16x16x128_f8f6f4 v[82:85], v[2:9], v[200:207], v[82:85], v188, v189 op_sel_hi:[0,0,0]
	v_mfma_scale_f32_16x16x128_f8f6f4 v[74:77], v[10:17], v[200:207], v[74:77], v188, v189 op_sel_hi:[0,0,0]
	v_mfma_scale_f32_16x16x128_f8f6f4 v[66:69], v[2:9], v[208:215], v[66:69], v188, v189 op_sel_hi:[0,0,0]
	v_mfma_scale_f32_16x16x128_f8f6f4 v[58:61], v[10:17], v[208:215], v[58:61], v188, v189 op_sel_hi:[0,0,0]
	v_mfma_scale_f32_16x16x128_f8f6f4 v[50:53], v[2:9], v[220:227], v[50:53], v188, v189 op_sel_hi:[0,0,0]
	v_mfma_scale_f32_16x16x128_f8f6f4 v[42:45], v[10:17], v[220:227], v[42:45], v188, v189 op_sel_hi:[0,0,0]
	v_mfma_scale_f32_16x16x128_f8f6f4 v[86:89], v[18:25], v[192:199], v[86:89], v188, v189 op_sel_hi:[0,0,0]
	v_mfma_scale_f32_16x16x128_f8f6f4 v[78:81], v[26:33], v[192:199], v[78:81], v188, v189 op_sel_hi:[0,0,0]
	v_mfma_scale_f32_16x16x128_f8f6f4 v[70:73], v[18:25], v[200:207], v[70:73], v188, v189 op_sel_hi:[0,0,0]
	v_mfma_scale_f32_16x16x128_f8f6f4 v[62:65], v[26:33], v[200:207], v[62:65], v188, v189 op_sel_hi:[0,0,0]
	v_mfma_scale_f32_16x16x128_f8f6f4 v[54:57], v[18:25], v[208:215], v[54:57], v188, v189 op_sel_hi:[0,0,0]
	v_mfma_scale_f32_16x16x128_f8f6f4 v[46:49], v[26:33], v[208:215], v[46:49], v188, v189 op_sel_hi:[0,0,0]
	v_mfma_scale_f32_16x16x128_f8f6f4 v[38:41], v[18:25], v[220:227], v[38:41], v188, v189 op_sel_hi:[0,0,0]
	v_mfma_scale_f32_16x16x128_f8f6f4 v[34:37], v[26:33], v[220:227], v[34:37], v188, v189 op_sel_hi:[0,0,0]
	s_barrier
	s_add_i32 s80, s80, 2
	s_add_u32 s74, s74, 0x10000
	s_addc_u32 s75, s75, 0
	s_add_u32 s56, s56, 0x100
	s_addc_u32 s57, s57, 0
	s_cmp_gt_u32 s80, 13
	s_cbranch_scc0 .LBB0_985
	s_and_b64 vcc, exec, s[24:25]
	s_cbranch_vccz .LBB0_988
	s_barrier

.LBB0_1192:
	ds_read_b128 v[66:69], v199
	ds_read_b128 v[70:73], v199 offset:1024
	ds_read_b128 v[82:85], v199 offset:2048
	ds_read_b128 v[86:89], v199 offset:3072
	ds_read_b128 v[146:149], v200
	ds_read_b128 v[150:153], v200 offset:1024
	ds_read_b128 v[154:157], v200 offset:2048
	ds_read_b128 v[158:161], v200 offset:3072
	s_add_u32 s26, s56, 0xfffc0080
	s_addc_u32 s27, s57, -1
	s_cmp_eq_u32 s73, 12
	s_cselect_b32 s59, s45, s27
	s_cselect_b32 s58, s69, s26
	s_cselect_b32 s27, s41, s72
	s_cselect_b32 s26, s70, s71
	v_lshl_add_u64 v[214:215], s[56:57], 0, v[176:177]
	s_add_i32 m0, s55, 0xc000
	ds_read_b128 v[162:165], v201
	ds_read_b128 v[166:169], v201 offset:1024
	ds_read_b128 v[184:187], v201 offset:2048
	ds_read_b128 v[188:191], v201 offset:3072
	ds_read_b128 v[192:195], v201 offset:4096
	ds_read_b128 v[202:205], v201 offset:5120
	ds_read_b128 v[206:209], v201 offset:6144
	ds_read_b128 v[210:213], v201 offset:7168
	global_load_lds_dwordx4 v[214:215], off
	v_lshl_add_u64 v[214:215], s[56:57], 0, v[178:179]
	s_add_i32 m0, s55, 0xe000
	s_nop 0
	global_load_lds_dwordx4 v[214:215], off
	s_waitcnt vmcnt(8)
	s_waitcnt lgkmcnt(0)
	s_barrier
	v_mfma_f32_16x16x32_bf16 v[142:145], v[66:69], v[162:165], v[142:145]
	v_mfma_f32_16x16x32_bf16 v[138:141], v[82:85], v[162:165], v[138:141]
	v_mfma_f32_16x16x32_bf16 v[126:129], v[66:69], v[184:187], v[126:129]
	v_mfma_f32_16x16x32_bf16 v[122:125], v[82:85], v[184:187], v[122:125]
	v_mfma_f32_16x16x32_bf16 v[110:113], v[66:69], v[192:195], v[110:113]
	v_mfma_f32_16x16x32_bf16 v[106:109], v[82:85], v[192:195], v[106:109]
	v_mfma_f32_16x16x32_bf16 v[94:97], v[66:69], v[206:209], v[94:97]
	v_mfma_f32_16x16x32_bf16 v[90:93], v[82:85], v[206:209], v[90:93]
	v_mfma_f32_16x16x32_bf16 v[142:145], v[70:73], v[166:169], v[142:145]
	v_mfma_f32_16x16x32_bf16 v[138:141], v[86:89], v[166:169], v[138:141]
	v_mfma_f32_16x16x32_bf16 v[126:129], v[70:73], v[188:191], v[126:129]
	v_mfma_f32_16x16x32_bf16 v[122:125], v[86:89], v[188:191], v[122:125]
	v_mfma_f32_16x16x32_bf16 v[110:113], v[70:73], v[202:205], v[110:113]
	v_mfma_f32_16x16x32_bf16 v[106:109], v[86:89], v[202:205], v[106:109]
	v_mfma_f32_16x16x32_bf16 v[94:97], v[70:73], v[210:213], v[94:97]
	v_mfma_f32_16x16x32_bf16 v[90:93], v[86:89], v[210:213], v[90:93]
	v_mfma_f32_16x16x32_bf16 v[134:137], v[146:149], v[162:165], v[134:137]
	v_mfma_f32_16x16x32_bf16 v[130:133], v[154:157], v[162:165], v[130:133]
	v_mfma_f32_16x16x32_bf16 v[118:121], v[146:149], v[184:187], v[118:121]
	v_mfma_f32_16x16x32_bf16 v[114:117], v[154:157], v[184:187], v[114:117]
	v_mfma_f32_16x16x32_bf16 v[102:105], v[146:149], v[192:195], v[102:105]
	v_mfma_f32_16x16x32_bf16 v[98:101], v[154:157], v[192:195], v[98:101]
	v_mfma_f32_16x16x32_bf16 v[78:81], v[146:149], v[206:209], v[78:81]
	v_mfma_f32_16x16x32_bf16 v[74:77], v[154:157], v[206:209], v[74:77]
	v_mfma_f32_16x16x32_bf16 v[134:137], v[150:153], v[166:169], v[134:137]
	v_mfma_f32_16x16x32_bf16 v[130:133], v[158:161], v[166:169], v[130:133]
	v_mfma_f32_16x16x32_bf16 v[118:121], v[150:153], v[188:191], v[118:121]
	v_mfma_f32_16x16x32_bf16 v[114:117], v[158:161], v[188:191], v[114:117]
	v_mfma_f32_16x16x32_bf16 v[102:105], v[150:153], v[202:205], v[102:105]
	v_mfma_f32_16x16x32_bf16 v[98:101], v[158:161], v[202:205], v[98:101]
	v_mfma_f32_16x16x32_bf16 v[78:81], v[150:153], v[210:213], v[78:81]
	v_mfma_f32_16x16x32_bf16 v[74:77], v[158:161], v[210:213], v[74:77]
	s_barrier
	v_lshl_add_u64 v[214:215], s[26:27], 0, v[170:171]
	s_add_i32 s26, s67, s35
	s_mov_b32 m0, s26
	ds_read_b128 v[162:165], v201 offset:16384
	ds_read_b128 v[166:169], v201 offset:17408
	ds_read_b128 v[184:187], v201 offset:18432
	ds_read_b128 v[188:191], v201 offset:19456
	ds_read_b128 v[192:195], v201 offset:20480
	ds_read_b128 v[202:205], v201 offset:21504
	ds_read_b128 v[206:209], v201 offset:22528
	ds_read_b128 v[210:213], v201 offset:23552
	global_load_lds_dwordx4 v[214:215], off
	v_lshl_add_u64 v[216:217], v[214:215], 0, s[6:7]
	s_add_i32 m0, s26, 0x2000
	s_add_i32 s26, s68, s35
	global_load_lds_dwordx4 v[216:217], off
	v_lshl_add_u64 v[216:217], v[214:215], 0, s[10:11]
	s_mov_b32 m0, s26
	v_lshl_add_u64 v[220:221], s[58:59], 0, v[174:175]
	global_load_lds_dwordx4 v[216:217], off
	v_lshl_add_u64 v[216:217], v[214:215], 0, s[12:13]
	s_add_i32 m0, s26, 0x2000
	s_nop 0
	global_load_lds_dwordx4 v[216:217], off
	v_lshl_add_u64 v[216:217], s[58:59], 0, v[172:173]
	s_mov_b32 m0, s55
	s_nop 0
	global_load_lds_dwordx4 v[216:217], off
	s_mov_b32 m0, s60
	s_nop 0
	global_load_lds_dwordx4 v[220:221], off
	s_waitcnt vmcnt(8)
	s_waitcnt lgkmcnt(0)
	s_barrier
	v_mfma_f32_16x16x32_bf16 v[62:65], v[66:69], v[162:165], v[62:65]
	v_mfma_f32_16x16x32_bf16 v[58:61], v[82:85], v[162:165], v[58:61]
	v_mfma_f32_16x16x32_bf16 v[46:49], v[66:69], v[184:187], v[46:49]
	v_mfma_f32_16x16x32_bf16 v[42:45], v[82:85], v[184:187], v[42:45]
	v_mfma_f32_16x16x32_bf16 v[30:33], v[66:69], v[192:195], v[30:33]
	v_mfma_f32_16x16x32_bf16 v[26:29], v[82:85], v[192:195], v[26:29]
	v_mfma_f32_16x16x32_bf16 v[14:17], v[66:69], v[206:209], v[14:17]
	v_mfma_f32_16x16x32_bf16 v[10:13], v[82:85], v[206:209], v[10:13]
	v_mfma_f32_16x16x32_bf16 v[62:65], v[70:73], v[166:169], v[62:65]
	v_mfma_f32_16x16x32_bf16 v[58:61], v[86:89], v[166:169], v[58:61]
	v_mfma_f32_16x16x32_bf16 v[46:49], v[70:73], v[188:191], v[46:49]
	v_mfma_f32_16x16x32_bf16 v[42:45], v[86:89], v[188:191], v[42:45]
	v_mfma_f32_16x16x32_bf16 v[30:33], v[70:73], v[202:205], v[30:33]
	v_mfma_f32_16x16x32_bf16 v[26:29], v[86:89], v[202:205], v[26:29]
	v_mfma_f32_16x16x32_bf16 v[14:17], v[70:73], v[210:213], v[14:17]
	v_mfma_f32_16x16x32_bf16 v[10:13], v[86:89], v[210:213], v[10:13]
	v_mfma_f32_16x16x32_bf16 v[54:57], v[146:149], v[162:165], v[54:57]
	v_mfma_f32_16x16x32_bf16 v[50:53], v[154:157], v[162:165], v[50:53]
	v_mfma_f32_16x16x32_bf16 v[38:41], v[146:149], v[184:187], v[38:41]
	v_mfma_f32_16x16x32_bf16 v[34:37], v[154:157], v[184:187], v[34:37]
	v_mfma_f32_16x16x32_bf16 v[22:25], v[146:149], v[192:195], v[22:25]
	v_mfma_f32_16x16x32_bf16 v[18:21], v[154:157], v[192:195], v[18:21]
	v_mfma_f32_16x16x32_bf16 v[6:9], v[146:149], v[206:209], v[6:9]
	v_mfma_f32_16x16x32_bf16 v[2:5], v[154:157], v[206:209], v[2:5]
	v_mfma_f32_16x16x32_bf16 v[54:57], v[150:153], v[166:169], v[54:57]
	v_mfma_f32_16x16x32_bf16 v[50:53], v[158:161], v[166:169], v[50:53]
	v_mfma_f32_16x16x32_bf16 v[38:41], v[150:153], v[188:191], v[38:41]
	v_mfma_f32_16x16x32_bf16 v[34:37], v[158:161], v[188:191], v[34:37]
	v_mfma_f32_16x16x32_bf16 v[22:25], v[150:153], v[202:205], v[22:25]
	v_mfma_f32_16x16x32_bf16 v[18:21], v[158:161], v[202:205], v[18:21]
	v_mfma_f32_16x16x32_bf16 v[6:9], v[150:153], v[210:213], v[6:9]
	v_mfma_f32_16x16x32_bf16 v[2:5], v[158:161], v[210:213], v[2:5]
	s_barrier
	s_add_i32 s74, 0, 0x18000
	s_add_i32 s75, 0, 0x1c000
	v_add_u32_e32 v86, s74, v197
	v_add_u32_e32 v158, s75, v197
	ds_read_b128 v[66:69], v86
	ds_read_b128 v[70:73], v86 offset:1024
	ds_read_b128 v[82:85], v86 offset:2048
	ds_read_b128 v[86:89], v86 offset:3072
	ds_read_b128 v[146:149], v158
	ds_read_b128 v[150:153], v158 offset:1024
	ds_read_b128 v[154:157], v158 offset:2048
	ds_read_b128 v[158:161], v158 offset:3072
	s_add_u32 s26, s58, 0x40000
	s_addc_u32 s27, s59, 0
	s_mov_b32 m0, s61
	v_lshl_add_u64 v[222:223], s[26:27], 0, v[172:173]
	ds_read_b128 v[162:165], v201 offset:32768
	ds_read_b128 v[166:169], v201 offset:33792
	ds_read_b128 v[184:187], v201 offset:34816
	ds_read_b128 v[188:191], v201 offset:35840
	ds_read_b128 v[192:195], v201 offset:36864
	ds_read_b128 v[202:205], v201 offset:37888
	ds_read_b128 v[206:209], v201 offset:38912
	ds_read_b128 v[210:213], v201 offset:39936
	global_load_lds_dwordx4 v[222:223], off
	v_lshl_add_u64 v[222:223], s[26:27], 0, v[174:175]
	s_mov_b32 m0, s62
	s_nop 0
	global_load_lds_dwordx4 v[222:223], off
	s_waitcnt vmcnt(8)
	s_waitcnt lgkmcnt(0)
	s_barrier
	v_mfma_f32_16x16x32_bf16 v[142:145], v[66:69], v[162:165], v[142:145]
	v_mfma_f32_16x16x32_bf16 v[138:141], v[82:85], v[162:165], v[138:141]
	v_mfma_f32_16x16x32_bf16 v[126:129], v[66:69], v[184:187], v[126:129]
	v_mfma_f32_16x16x32_bf16 v[122:125], v[82:85], v[184:187], v[122:125]
	v_mfma_f32_16x16x32_bf16 v[110:113], v[66:69], v[192:195], v[110:113]
	v_mfma_f32_16x16x32_bf16 v[106:109], v[82:85], v[192:195], v[106:109]
	v_mfma_f32_16x16x32_bf16 v[94:97], v[66:69], v[206:209], v[94:97]
	v_mfma_f32_16x16x32_bf16 v[90:93], v[82:85], v[206:209], v[90:93]
	v_mfma_f32_16x16x32_bf16 v[142:145], v[70:73], v[166:169], v[142:145]
	v_mfma_f32_16x16x32_bf16 v[138:141], v[86:89], v[166:169], v[138:141]
	v_mfma_f32_16x16x32_bf16 v[126:129], v[70:73], v[188:191], v[126:129]
	v_mfma_f32_16x16x32_bf16 v[122:125], v[86:89], v[188:191], v[122:125]
	v_mfma_f32_16x16x32_bf16 v[110:113], v[70:73], v[202:205], v[110:113]
	v_mfma_f32_16x16x32_bf16 v[106:109], v[86:89], v[202:205], v[106:109]
	v_mfma_f32_16x16x32_bf16 v[94:97], v[70:73], v[210:213], v[94:97]
	v_mfma_f32_16x16x32_bf16 v[90:93], v[86:89], v[210:213], v[90:93]
	v_mfma_f32_16x16x32_bf16 v[134:137], v[146:149], v[162:165], v[134:137]
	v_mfma_f32_16x16x32_bf16 v[130:133], v[154:157], v[162:165], v[130:133]
	v_mfma_f32_16x16x32_bf16 v[118:121], v[146:149], v[184:187], v[118:121]
	v_mfma_f32_16x16x32_bf16 v[114:117], v[154:157], v[184:187], v[114:117]
	v_mfma_f32_16x16x32_bf16 v[102:105], v[146:149], v[192:195], v[102:105]
	v_mfma_f32_16x16x32_bf16 v[98:101], v[154:157], v[192:195], v[98:101]
	v_mfma_f32_16x16x32_bf16 v[78:81], v[146:149], v[206:209], v[78:81]
	v_mfma_f32_16x16x32_bf16 v[74:77], v[154:157], v[206:209], v[74:77]
	v_mfma_f32_16x16x32_bf16 v[134:137], v[150:153], v[166:169], v[134:137]
	v_mfma_f32_16x16x32_bf16 v[130:133], v[158:161], v[166:169], v[130:133]
	v_mfma_f32_16x16x32_bf16 v[118:121], v[150:153], v[188:191], v[118:121]
	v_mfma_f32_16x16x32_bf16 v[114:117], v[158:161], v[188:191], v[114:117]
	v_mfma_f32_16x16x32_bf16 v[102:105], v[150:153], v[202:205], v[102:105]
	v_mfma_f32_16x16x32_bf16 v[98:101], v[158:161], v[202:205], v[98:101]
	v_mfma_f32_16x16x32_bf16 v[78:81], v[150:153], v[210:213], v[78:81]
	v_mfma_f32_16x16x32_bf16 v[74:77], v[158:161], v[210:213], v[74:77]
	s_barrier
	s_add_i32 s26, s74, s35
	v_lshl_add_u64 v[222:223], v[214:215], 0, s[16:17]
	s_mov_b32 m0, s26
	ds_read_b128 v[162:165], v201 offset:49152
	ds_read_b128 v[166:169], v201 offset:50176
	ds_read_b128 v[184:187], v201 offset:51200
	ds_read_b128 v[188:191], v201 offset:52224
	ds_read_b128 v[192:195], v201 offset:53248
	ds_read_b128 v[202:205], v201 offset:54272
	ds_read_b128 v[206:209], v201 offset:55296
	ds_read_b128 v[210:213], v201 offset:56320
	global_load_lds_dwordx4 v[222:223], off
	v_lshl_add_u64 v[222:223], v[214:215], 0, s[18:19]
	s_add_i32 m0, s26, 0x2000
	s_add_i32 s26, s75, s35
	global_load_lds_dwordx4 v[222:223], off
	v_lshl_add_u64 v[222:223], v[214:215], 0, s[22:23]
	s_mov_b32 m0, s26
	v_lshl_add_u64 v[214:215], v[214:215], 0, s[24:25]
	global_load_lds_dwordx4 v[222:223], off
	s_add_i32 m0, s26, 0x2000
	s_nop 0
	global_load_lds_dwordx4 v[214:215], off
	v_lshl_add_u64 v[214:215], v[216:217], 0, s[20:21]
	s_mov_b32 m0, s64
	s_nop 0
	global_load_lds_dwordx4 v[214:215], off
	v_lshl_add_u64 v[214:215], v[220:221], 0, s[20:21]
	s_mov_b32 m0, s65
	s_nop 0
	global_load_lds_dwordx4 v[214:215], off
	s_waitcnt vmcnt(8)
	s_waitcnt lgkmcnt(0)
	s_barrier
	v_mfma_f32_16x16x32_bf16 v[62:65], v[66:69], v[162:165], v[62:65]
	v_mfma_f32_16x16x32_bf16 v[58:61], v[82:85], v[162:165], v[58:61]
	v_mfma_f32_16x16x32_bf16 v[46:49], v[66:69], v[184:187], v[46:49]
	v_mfma_f32_16x16x32_bf16 v[42:45], v[82:85], v[184:187], v[42:45]
	v_mfma_f32_16x16x32_bf16 v[30:33], v[66:69], v[192:195], v[30:33]
	v_mfma_f32_16x16x32_bf16 v[26:29], v[82:85], v[192:195], v[26:29]
	v_mfma_f32_16x16x32_bf16 v[14:17], v[66:69], v[206:209], v[14:17]
	v_mfma_f32_16x16x32_bf16 v[10:13], v[82:85], v[206:209], v[10:13]
	v_mfma_f32_16x16x32_bf16 v[62:65], v[70:73], v[166:169], v[62:65]
	v_mfma_f32_16x16x32_bf16 v[58:61], v[86:89], v[166:169], v[58:61]
	v_mfma_f32_16x16x32_bf16 v[46:49], v[70:73], v[188:191], v[46:49]
	v_mfma_f32_16x16x32_bf16 v[42:45], v[86:89], v[188:191], v[42:45]
	v_mfma_f32_16x16x32_bf16 v[30:33], v[70:73], v[202:205], v[30:33]
	v_mfma_f32_16x16x32_bf16 v[26:29], v[86:89], v[202:205], v[26:29]
	v_mfma_f32_16x16x32_bf16 v[14:17], v[70:73], v[210:213], v[14:17]
	v_mfma_f32_16x16x32_bf16 v[10:13], v[86:89], v[210:213], v[10:13]
	v_mfma_f32_16x16x32_bf16 v[54:57], v[146:149], v[162:165], v[54:57]
	v_mfma_f32_16x16x32_bf16 v[50:53], v[154:157], v[162:165], v[50:53]
	v_mfma_f32_16x16x32_bf16 v[38:41], v[146:149], v[184:187], v[38:41]
	v_mfma_f32_16x16x32_bf16 v[34:37], v[154:157], v[184:187], v[34:37]
	v_mfma_f32_16x16x32_bf16 v[22:25], v[146:149], v[192:195], v[22:25]
	v_mfma_f32_16x16x32_bf16 v[18:21], v[154:157], v[192:195], v[18:21]
	v_mfma_f32_16x16x32_bf16 v[6:9], v[146:149], v[206:209], v[6:9]
	v_mfma_f32_16x16x32_bf16 v[2:5], v[154:157], v[206:209], v[2:5]
	v_mfma_f32_16x16x32_bf16 v[54:57], v[150:153], v[166:169], v[54:57]
	v_mfma_f32_16x16x32_bf16 v[50:53], v[158:161], v[166:169], v[50:53]
	v_mfma_f32_16x16x32_bf16 v[38:41], v[150:153], v[188:191], v[38:41]
	v_mfma_f32_16x16x32_bf16 v[34:37], v[158:161], v[188:191], v[34:37]
	v_mfma_f32_16x16x32_bf16 v[22:25], v[150:153], v[202:205], v[22:25]
	v_mfma_f32_16x16x32_bf16 v[18:21], v[158:161], v[202:205], v[18:21]
	v_mfma_f32_16x16x32_bf16 v[6:9], v[150:153], v[210:213], v[6:9]
	v_mfma_f32_16x16x32_bf16 v[2:5], v[158:161], v[210:213], v[2:5]
	s_barrier
	s_add_i32 s73, s73, 2
	s_add_u32 s71, s71, 0x10000
	s_addc_u32 s72, s72, 0
	s_add_u32 s56, s56, 0x100
	s_addc_u32 s57, s57, 0
	s_cmp_gt_u32 s73, 13
	s_cbranch_scc0 .LBB0_1192
	s_and_b64 vcc, exec, s[36:37]
	s_cbranch_vccz .LBB0_1195
	s_barrier

.LBB0_1271:
	ds_read_b128 v[144:147], v158
	ds_read_b128 v[148:151], v158 offset:1024
	ds_read_b128 v[152:155], v158 offset:2048
	ds_read_b128 v[162:165], v158 offset:3072
	ds_read_b128 v[166:169], v159
	ds_read_b128 v[170:173], v159 offset:1024
	ds_read_b128 v[174:177], v159 offset:2048
	ds_read_b128 v[178:181], v159 offset:3072
	s_add_u32 s26, s58, 0xfff80080
	s_addc_u32 s27, s59, -1
	s_cmp_eq_u32 s80, 28
	s_cselect_b32 s61, s51, s27
	s_cselect_b32 s60, s57, s26
	s_cselect_b32 s27, s45, s75
	s_cselect_b32 s26, s73, s74
	v_lshl_add_u64 v[214:215], s[58:59], 0, v[136:137]
	s_add_i32 m0, s63, 0xc000
	ds_read_b128 v[182:185], v160
	ds_read_b128 v[186:189], v160 offset:1024
	ds_read_b128 v[190:193], v160 offset:2048
	ds_read_b128 v[194:197], v160 offset:3072
	ds_read_b128 v[198:201], v160 offset:4096
	ds_read_b128 v[202:205], v160 offset:5120
	ds_read_b128 v[206:209], v160 offset:6144
	ds_read_b128 v[210:213], v160 offset:7168
	global_load_lds_dwordx4 v[214:215], off
	v_lshl_add_u64 v[214:215], s[58:59], 0, v[138:139]
	s_add_i32 m0, s63, 0xe000
	s_nop 0
	global_load_lds_dwordx4 v[214:215], off
	s_waitcnt vmcnt(8)
	s_waitcnt lgkmcnt(0)
	s_barrier
	v_mfma_f32_16x16x32_bf16 v[126:129], v[144:147], v[182:185], v[126:129]
	v_mfma_f32_16x16x32_bf16 v[122:125], v[152:155], v[182:185], v[122:125]
	v_mfma_f32_16x16x32_bf16 v[118:121], v[144:147], v[190:193], v[118:121]
	v_mfma_f32_16x16x32_bf16 v[114:117], v[152:155], v[190:193], v[114:117]
	v_mfma_f32_16x16x32_bf16 v[106:109], v[144:147], v[198:201], v[106:109]
	v_mfma_f32_16x16x32_bf16 v[98:101], v[152:155], v[198:201], v[98:101]
	v_mfma_f32_16x16x32_bf16 v[90:93], v[144:147], v[206:209], v[90:93]
	v_mfma_f32_16x16x32_bf16 v[82:85], v[152:155], v[206:209], v[82:85]
	v_mfma_f32_16x16x32_bf16 v[126:129], v[148:151], v[186:189], v[126:129]
	v_mfma_f32_16x16x32_bf16 v[122:125], v[162:165], v[186:189], v[122:125]
	v_mfma_f32_16x16x32_bf16 v[118:121], v[148:151], v[194:197], v[118:121]
	v_mfma_f32_16x16x32_bf16 v[114:117], v[162:165], v[194:197], v[114:117]
	v_mfma_f32_16x16x32_bf16 v[106:109], v[148:151], v[202:205], v[106:109]
	v_mfma_f32_16x16x32_bf16 v[98:101], v[162:165], v[202:205], v[98:101]
	v_mfma_f32_16x16x32_bf16 v[90:93], v[148:151], v[210:213], v[90:93]
	v_mfma_f32_16x16x32_bf16 v[82:85], v[162:165], v[210:213], v[82:85]
	v_mfma_f32_16x16x32_bf16 v[110:113], v[166:169], v[182:185], v[110:113]
	v_mfma_f32_16x16x32_bf16 v[102:105], v[174:177], v[182:185], v[102:105]
	v_mfma_f32_16x16x32_bf16 v[94:97], v[166:169], v[190:193], v[94:97]
	v_mfma_f32_16x16x32_bf16 v[86:89], v[174:177], v[190:193], v[86:89]
	v_mfma_f32_16x16x32_bf16 v[78:81], v[166:169], v[198:201], v[78:81]
	v_mfma_f32_16x16x32_bf16 v[74:77], v[174:177], v[198:201], v[74:77]
	v_mfma_f32_16x16x32_bf16 v[70:73], v[166:169], v[206:209], v[70:73]
	v_mfma_f32_16x16x32_bf16 v[66:69], v[174:177], v[206:209], v[66:69]
	v_mfma_f32_16x16x32_bf16 v[110:113], v[170:173], v[186:189], v[110:113]
	v_mfma_f32_16x16x32_bf16 v[102:105], v[178:181], v[186:189], v[102:105]
	v_mfma_f32_16x16x32_bf16 v[94:97], v[170:173], v[194:197], v[94:97]
	v_mfma_f32_16x16x32_bf16 v[86:89], v[178:181], v[194:197], v[86:89]
	v_mfma_f32_16x16x32_bf16 v[78:81], v[170:173], v[202:205], v[78:81]
	v_mfma_f32_16x16x32_bf16 v[74:77], v[178:181], v[202:205], v[74:77]
	v_mfma_f32_16x16x32_bf16 v[70:73], v[170:173], v[210:213], v[70:73]
	v_mfma_f32_16x16x32_bf16 v[66:69], v[178:181], v[210:213], v[66:69]
	s_barrier
	v_lshl_add_u64 v[214:215], s[26:27], 0, v[130:131]
	s_add_i32 s26, s71, s35
	s_mov_b32 m0, s26
	ds_read_b128 v[182:185], v160 offset:16384
	ds_read_b128 v[186:189], v160 offset:17408
	ds_read_b128 v[190:193], v160 offset:18432
	ds_read_b128 v[194:197], v160 offset:19456
	ds_read_b128 v[198:201], v160 offset:20480
	ds_read_b128 v[202:205], v160 offset:21504
	ds_read_b128 v[206:209], v160 offset:22528
	ds_read_b128 v[210:213], v160 offset:23552
	global_load_lds_dwordx4 v[214:215], off
	v_lshl_add_u64 v[216:217], v[214:215], 0, s[6:7]
	s_add_i32 m0, s26, 0x2000
	s_add_i32 s26, s72, s35
	global_load_lds_dwordx4 v[216:217], off
	v_lshl_add_u64 v[216:217], v[214:215], 0, s[8:9]
	s_mov_b32 m0, s26
	v_lshl_add_u64 v[220:221], s[60:61], 0, v[134:135]
	global_load_lds_dwordx4 v[216:217], off
	v_lshl_add_u64 v[216:217], v[214:215], 0, s[10:11]
	s_add_i32 m0, s26, 0x2000
	s_nop 0
	global_load_lds_dwordx4 v[216:217], off
	v_lshl_add_u64 v[216:217], s[60:61], 0, v[132:133]
	s_mov_b32 m0, s63
	s_nop 0
	global_load_lds_dwordx4 v[216:217], off
	s_mov_b32 m0, s64
	s_nop 0
	global_load_lds_dwordx4 v[220:221], off
	s_waitcnt vmcnt(8)
	s_waitcnt lgkmcnt(0)
	s_barrier
	v_mfma_f32_16x16x32_bf16 v[62:65], v[144:147], v[182:185], v[62:65]
	v_mfma_f32_16x16x32_bf16 v[58:61], v[152:155], v[182:185], v[58:61]
	v_mfma_f32_16x16x32_bf16 v[54:57], v[144:147], v[190:193], v[54:57]
	v_mfma_f32_16x16x32_bf16 v[46:49], v[152:155], v[190:193], v[46:49]
	v_mfma_f32_16x16x32_bf16 v[38:41], v[144:147], v[198:201], v[38:41]
	v_mfma_f32_16x16x32_bf16 v[30:33], v[152:155], v[198:201], v[30:33]
	v_mfma_f32_16x16x32_bf16 v[22:25], v[144:147], v[206:209], v[22:25]
	v_mfma_f32_16x16x32_bf16 v[14:17], v[152:155], v[206:209], v[14:17]
	v_mfma_f32_16x16x32_bf16 v[62:65], v[148:151], v[186:189], v[62:65]
	v_mfma_f32_16x16x32_bf16 v[58:61], v[162:165], v[186:189], v[58:61]
	v_mfma_f32_16x16x32_bf16 v[54:57], v[148:151], v[194:197], v[54:57]
	v_mfma_f32_16x16x32_bf16 v[46:49], v[162:165], v[194:197], v[46:49]
	v_mfma_f32_16x16x32_bf16 v[38:41], v[148:151], v[202:205], v[38:41]
	v_mfma_f32_16x16x32_bf16 v[30:33], v[162:165], v[202:205], v[30:33]
	v_mfma_f32_16x16x32_bf16 v[22:25], v[148:151], v[210:213], v[22:25]
	v_mfma_f32_16x16x32_bf16 v[14:17], v[162:165], v[210:213], v[14:17]
	v_mfma_f32_16x16x32_bf16 v[50:53], v[166:169], v[182:185], v[50:53]
	v_mfma_f32_16x16x32_bf16 v[42:45], v[174:177], v[182:185], v[42:45]
	v_mfma_f32_16x16x32_bf16 v[34:37], v[166:169], v[190:193], v[34:37]
	v_mfma_f32_16x16x32_bf16 v[26:29], v[174:177], v[190:193], v[26:29]
	v_mfma_f32_16x16x32_bf16 v[18:21], v[166:169], v[198:201], v[18:21]
	v_mfma_f32_16x16x32_bf16 v[10:13], v[174:177], v[198:201], v[10:13]
	v_mfma_f32_16x16x32_bf16 v[6:9], v[166:169], v[206:209], v[6:9]
	v_mfma_f32_16x16x32_bf16 v[2:5], v[174:177], v[206:209], v[2:5]
	v_mfma_f32_16x16x32_bf16 v[50:53], v[170:173], v[186:189], v[50:53]
	v_mfma_f32_16x16x32_bf16 v[42:45], v[178:181], v[186:189], v[42:45]
	v_mfma_f32_16x16x32_bf16 v[34:37], v[170:173], v[194:197], v[34:37]
	v_mfma_f32_16x16x32_bf16 v[26:29], v[178:181], v[194:197], v[26:29]
	v_mfma_f32_16x16x32_bf16 v[18:21], v[170:173], v[202:205], v[18:21]
	v_mfma_f32_16x16x32_bf16 v[10:13], v[178:181], v[202:205], v[10:13]
	v_mfma_f32_16x16x32_bf16 v[6:9], v[170:173], v[210:213], v[6:9]
	v_mfma_f32_16x16x32_bf16 v[2:5], v[178:181], v[210:213], v[2:5]
	s_barrier
	s_add_i32 s81, 0, 0x18000
	v_add_u32_e32 v161, s81, v156
	s_add_i32 s82, 0, 0x1c000
	ds_read_b128 v[144:147], v161
	ds_read_b128 v[148:151], v161 offset:1024
	ds_read_b128 v[152:155], v161 offset:2048
	ds_read_b128 v[162:165], v161 offset:3072
	v_add_u32_e32 v161, s82, v156
	ds_read_b128 v[166:169], v161
	ds_read_b128 v[170:173], v161 offset:1024
	ds_read_b128 v[174:177], v161 offset:2048
	ds_read_b128 v[178:181], v161 offset:3072
	s_add_u32 s26, s60, 0x80000
	s_addc_u32 s27, s61, 0
	s_mov_b32 m0, s65
	v_lshl_add_u64 v[222:223], s[26:27], 0, v[132:133]
	ds_read_b128 v[182:185], v160 offset:32768
	ds_read_b128 v[186:189], v160 offset:33792
	ds_read_b128 v[190:193], v160 offset:34816
	ds_read_b128 v[194:197], v160 offset:35840
	ds_read_b128 v[198:201], v160 offset:36864
	ds_read_b128 v[202:205], v160 offset:37888
	ds_read_b128 v[206:209], v160 offset:38912
	ds_read_b128 v[210:213], v160 offset:39936
	global_load_lds_dwordx4 v[222:223], off
	v_lshl_add_u64 v[222:223], s[26:27], 0, v[134:135]
	s_mov_b32 m0, s66
	s_nop 0
	global_load_lds_dwordx4 v[222:223], off
	s_waitcnt vmcnt(8)
	s_waitcnt lgkmcnt(0)
	s_barrier
	v_mfma_f32_16x16x32_bf16 v[126:129], v[144:147], v[182:185], v[126:129]
	v_mfma_f32_16x16x32_bf16 v[122:125], v[152:155], v[182:185], v[122:125]
	v_mfma_f32_16x16x32_bf16 v[118:121], v[144:147], v[190:193], v[118:121]
	v_mfma_f32_16x16x32_bf16 v[114:117], v[152:155], v[190:193], v[114:117]
	v_mfma_f32_16x16x32_bf16 v[106:109], v[144:147], v[198:201], v[106:109]
	v_mfma_f32_16x16x32_bf16 v[98:101], v[152:155], v[198:201], v[98:101]
	v_mfma_f32_16x16x32_bf16 v[90:93], v[144:147], v[206:209], v[90:93]
	v_mfma_f32_16x16x32_bf16 v[82:85], v[152:155], v[206:209], v[82:85]
	v_mfma_f32_16x16x32_bf16 v[126:129], v[148:151], v[186:189], v[126:129]
	v_mfma_f32_16x16x32_bf16 v[122:125], v[162:165], v[186:189], v[122:125]
	v_mfma_f32_16x16x32_bf16 v[118:121], v[148:151], v[194:197], v[118:121]
	v_mfma_f32_16x16x32_bf16 v[114:117], v[162:165], v[194:197], v[114:117]
	v_mfma_f32_16x16x32_bf16 v[106:109], v[148:151], v[202:205], v[106:109]
	v_mfma_f32_16x16x32_bf16 v[98:101], v[162:165], v[202:205], v[98:101]
	v_mfma_f32_16x16x32_bf16 v[90:93], v[148:151], v[210:213], v[90:93]
	v_mfma_f32_16x16x32_bf16 v[82:85], v[162:165], v[210:213], v[82:85]
	v_mfma_f32_16x16x32_bf16 v[110:113], v[166:169], v[182:185], v[110:113]
	v_mfma_f32_16x16x32_bf16 v[102:105], v[174:177], v[182:185], v[102:105]
	v_mfma_f32_16x16x32_bf16 v[94:97], v[166:169], v[190:193], v[94:97]
	v_mfma_f32_16x16x32_bf16 v[86:89], v[174:177], v[190:193], v[86:89]
	v_mfma_f32_16x16x32_bf16 v[78:81], v[166:169], v[198:201], v[78:81]
	v_mfma_f32_16x16x32_bf16 v[74:77], v[174:177], v[198:201], v[74:77]
	v_mfma_f32_16x16x32_bf16 v[70:73], v[166:169], v[206:209], v[70:73]
	v_mfma_f32_16x16x32_bf16 v[66:69], v[174:177], v[206:209], v[66:69]
	v_mfma_f32_16x16x32_bf16 v[110:113], v[170:173], v[186:189], v[110:113]
	v_mfma_f32_16x16x32_bf16 v[102:105], v[178:181], v[186:189], v[102:105]
	v_mfma_f32_16x16x32_bf16 v[94:97], v[170:173], v[194:197], v[94:97]
	v_mfma_f32_16x16x32_bf16 v[86:89], v[178:181], v[194:197], v[86:89]
	v_mfma_f32_16x16x32_bf16 v[78:81], v[170:173], v[202:205], v[78:81]
	v_mfma_f32_16x16x32_bf16 v[74:77], v[178:181], v[202:205], v[74:77]
	v_mfma_f32_16x16x32_bf16 v[70:73], v[170:173], v[210:213], v[70:73]
	v_mfma_f32_16x16x32_bf16 v[66:69], v[178:181], v[210:213], v[66:69]
	s_barrier
	s_add_i32 s26, s81, s35
	v_lshl_add_u64 v[222:223], v[214:215], 0, s[14:15]
	s_mov_b32 m0, s26
	ds_read_b128 v[182:185], v160 offset:49152
	ds_read_b128 v[186:189], v160 offset:50176
	ds_read_b128 v[190:193], v160 offset:51200
	ds_read_b128 v[194:197], v160 offset:52224
	ds_read_b128 v[198:201], v160 offset:53248
	ds_read_b128 v[202:205], v160 offset:54272
	ds_read_b128 v[206:209], v160 offset:55296
	ds_read_b128 v[210:213], v160 offset:56320
	global_load_lds_dwordx4 v[222:223], off
	v_lshl_add_u64 v[222:223], v[214:215], 0, s[16:17]
	s_add_i32 m0, s26, 0x2000
	s_add_i32 s26, s82, s35
	global_load_lds_dwordx4 v[222:223], off
	v_lshl_add_u64 v[222:223], v[214:215], 0, s[20:21]
	s_mov_b32 m0, s26
	v_lshl_add_u64 v[214:215], v[214:215], 0, s[22:23]
	global_load_lds_dwordx4 v[222:223], off
	s_add_i32 m0, s26, 0x2000
	s_nop 0
	global_load_lds_dwordx4 v[214:215], off
	v_lshl_add_u64 v[214:215], v[216:217], 0, s[18:19]
	s_mov_b32 m0, s68
	s_nop 0
	global_load_lds_dwordx4 v[214:215], off
	v_lshl_add_u64 v[214:215], v[220:221], 0, s[18:19]
	s_mov_b32 m0, s69
	s_nop 0
	global_load_lds_dwordx4 v[214:215], off
	s_waitcnt vmcnt(8)
	s_waitcnt lgkmcnt(0)
	s_barrier
	v_mfma_f32_16x16x32_bf16 v[62:65], v[144:147], v[182:185], v[62:65]
	v_mfma_f32_16x16x32_bf16 v[58:61], v[152:155], v[182:185], v[58:61]
	v_mfma_f32_16x16x32_bf16 v[54:57], v[144:147], v[190:193], v[54:57]
	v_mfma_f32_16x16x32_bf16 v[46:49], v[152:155], v[190:193], v[46:49]
	v_mfma_f32_16x16x32_bf16 v[38:41], v[144:147], v[198:201], v[38:41]
	v_mfma_f32_16x16x32_bf16 v[30:33], v[152:155], v[198:201], v[30:33]
	v_mfma_f32_16x16x32_bf16 v[22:25], v[144:147], v[206:209], v[22:25]
	v_mfma_f32_16x16x32_bf16 v[14:17], v[152:155], v[206:209], v[14:17]
	v_mfma_f32_16x16x32_bf16 v[62:65], v[148:151], v[186:189], v[62:65]
	v_mfma_f32_16x16x32_bf16 v[58:61], v[162:165], v[186:189], v[58:61]
	v_mfma_f32_16x16x32_bf16 v[54:57], v[148:151], v[194:197], v[54:57]
	v_mfma_f32_16x16x32_bf16 v[46:49], v[162:165], v[194:197], v[46:49]
	v_mfma_f32_16x16x32_bf16 v[38:41], v[148:151], v[202:205], v[38:41]
	v_mfma_f32_16x16x32_bf16 v[30:33], v[162:165], v[202:205], v[30:33]
	v_mfma_f32_16x16x32_bf16 v[22:25], v[148:151], v[210:213], v[22:25]
	v_mfma_f32_16x16x32_bf16 v[14:17], v[162:165], v[210:213], v[14:17]
	v_mfma_f32_16x16x32_bf16 v[50:53], v[166:169], v[182:185], v[50:53]
	v_mfma_f32_16x16x32_bf16 v[42:45], v[174:177], v[182:185], v[42:45]
	v_mfma_f32_16x16x32_bf16 v[34:37], v[166:169], v[190:193], v[34:37]
	v_mfma_f32_16x16x32_bf16 v[26:29], v[174:177], v[190:193], v[26:29]
	v_mfma_f32_16x16x32_bf16 v[18:21], v[166:169], v[198:201], v[18:21]
	v_mfma_f32_16x16x32_bf16 v[10:13], v[174:177], v[198:201], v[10:13]
	v_mfma_f32_16x16x32_bf16 v[6:9], v[166:169], v[206:209], v[6:9]
	v_mfma_f32_16x16x32_bf16 v[2:5], v[174:177], v[206:209], v[2:5]
	v_mfma_f32_16x16x32_bf16 v[50:53], v[170:173], v[186:189], v[50:53]
	v_mfma_f32_16x16x32_bf16 v[42:45], v[178:181], v[186:189], v[42:45]
	v_mfma_f32_16x16x32_bf16 v[34:37], v[170:173], v[194:197], v[34:37]
	v_mfma_f32_16x16x32_bf16 v[26:29], v[178:181], v[194:197], v[26:29]
	v_mfma_f32_16x16x32_bf16 v[18:21], v[170:173], v[202:205], v[18:21]
	v_mfma_f32_16x16x32_bf16 v[10:13], v[178:181], v[202:205], v[10:13]
	v_mfma_f32_16x16x32_bf16 v[6:9], v[170:173], v[210:213], v[6:9]
	v_mfma_f32_16x16x32_bf16 v[2:5], v[178:181], v[210:213], v[2:5]
	s_barrier
	s_add_i32 s80, s80, 2
	s_add_u32 s74, s74, 0x10000
	s_addc_u32 s75, s75, 0
	s_add_u32 s58, s58, 0x100
	s_addc_u32 s59, s59, 0
	s_cmp_gt_u32 s80, 29
	s_cbranch_scc0 .LBB0_1271
	s_and_b64 vcc, exec, s[24:25]
	s_cbranch_vccz .LBB0_1274
	s_barrier

.LBB0_1497:
	ds_read_b128 v[26:29], v186
	ds_read_b128 v[30:33], v186 offset:1024
	ds_read_b128 v[18:21], v186 offset:2048
	ds_read_b128 v[22:25], v186 offset:3072
	ds_read_b128 v[10:13], v187
	ds_read_b128 v[14:17], v187 offset:1024
	ds_read_b128 v[2:5], v187 offset:2048
	ds_read_b128 v[6:9], v187 offset:3072
	s_add_u32 s56, s4, 0xfffc0080
	s_addc_u32 s57, s5, -1
	s_cmp_eq_u32 s49, 12
	s_cselect_b64 vcc, -1, 0
	s_cselect_b32 s57, s2, s57
	s_cselect_b32 s56, s47, s56
	v_cndmask_b32_e32 v179, v177, v175, vcc
	v_cndmask_b32_e32 v178, v176, v174, vcc
	v_lshl_add_u64 v[180:181], s[4:5], 0, v[168:169]
	s_add_i32 m0, s62, 0xc000
	ds_read_b128 v[192:195], v188
	ds_read_b128 v[196:199], v188 offset:1024
	ds_read_b128 v[200:203], v188 offset:2048
	ds_read_b128 v[204:207], v188 offset:3072
	ds_read_b128 v[208:211], v188 offset:4096
	ds_read_b128 v[212:215], v188 offset:5120
	ds_read_b128 v[220:223], v188 offset:6144
	ds_read_b128 v[224:227], v188 offset:7168
	global_load_lds_dwordx4 v[180:181], off
	v_lshl_add_u64 v[180:181], s[4:5], 0, v[170:171]
	s_add_i32 m0, s62, 0xe000
	s_nop 0
	global_load_lds_dwordx4 v[180:181], off
	s_waitcnt vmcnt(8)
	s_waitcnt lgkmcnt(0)
	s_barrier
	v_mfma_scale_f32_16x16x128_f8f6f4 v[158:161], v[26:33], v[192:199], v[158:161], v189, v190 op_sel_hi:[0,0,0]
	v_mfma_scale_f32_16x16x128_f8f6f4 v[150:153], v[18:25], v[192:199], v[150:153], v189, v190 op_sel_hi:[0,0,0]
	v_mfma_scale_f32_16x16x128_f8f6f4 v[142:145], v[26:33], v[200:207], v[142:145], v189, v190 op_sel_hi:[0,0,0]
	v_mfma_scale_f32_16x16x128_f8f6f4 v[134:137], v[18:25], v[200:207], v[134:137], v189, v190 op_sel_hi:[0,0,0]
	v_mfma_scale_f32_16x16x128_f8f6f4 v[126:129], v[26:33], v[208:215], v[126:129], v189, v190 op_sel_hi:[0,0,0]
	v_mfma_scale_f32_16x16x128_f8f6f4 v[118:121], v[18:25], v[208:215], v[118:121], v189, v190 op_sel_hi:[0,0,0]
	v_mfma_scale_f32_16x16x128_f8f6f4 v[110:113], v[26:33], v[220:227], v[110:113], v189, v190 op_sel_hi:[0,0,0]
	v_mfma_scale_f32_16x16x128_f8f6f4 v[102:105], v[18:25], v[220:227], v[102:105], v189, v190 op_sel_hi:[0,0,0]
	v_mfma_scale_f32_16x16x128_f8f6f4 v[154:157], v[10:17], v[192:199], v[154:157], v189, v190 op_sel_hi:[0,0,0]
	v_mfma_scale_f32_16x16x128_f8f6f4 v[146:149], v[2:9], v[192:199], v[146:149], v189, v190 op_sel_hi:[0,0,0]
	v_mfma_scale_f32_16x16x128_f8f6f4 v[138:141], v[10:17], v[200:207], v[138:141], v189, v190 op_sel_hi:[0,0,0]
	v_mfma_scale_f32_16x16x128_f8f6f4 v[130:133], v[2:9], v[200:207], v[130:133], v189, v190 op_sel_hi:[0,0,0]
	v_mfma_scale_f32_16x16x128_f8f6f4 v[122:125], v[10:17], v[208:215], v[122:125], v189, v190 op_sel_hi:[0,0,0]
	v_mfma_scale_f32_16x16x128_f8f6f4 v[114:117], v[2:9], v[208:215], v[114:117], v189, v190 op_sel_hi:[0,0,0]
	v_mfma_scale_f32_16x16x128_f8f6f4 v[106:109], v[10:17], v[220:227], v[106:109], v189, v190 op_sel_hi:[0,0,0]
	v_mfma_scale_f32_16x16x128_f8f6f4 v[98:101], v[2:9], v[220:227], v[98:101], v189, v190 op_sel_hi:[0,0,0]
	s_barrier
	s_add_i32 s73, s69, s61
	v_lshl_add_u64 v[178:179], v[178:179], 0, v[162:163]
	s_mov_b32 m0, s73
	ds_read_b128 v[192:195], v188 offset:16384
	ds_read_b128 v[196:199], v188 offset:17408
	ds_read_b128 v[200:203], v188 offset:18432
	ds_read_b128 v[204:207], v188 offset:19456
	ds_read_b128 v[208:211], v188 offset:20480
	ds_read_b128 v[212:215], v188 offset:21504
	ds_read_b128 v[220:223], v188 offset:22528
	ds_read_b128 v[224:227], v188 offset:23552
	global_load_lds_dwordx4 v[178:179], off
	v_lshl_add_u64 v[180:181], v[178:179], 0, s[10:11]
	s_add_i32 m0, s73, 0x2000
	s_add_i32 s73, s70, s61
	global_load_lds_dwordx4 v[180:181], off
	v_lshl_add_u64 v[180:181], v[178:179], 0, s[12:13]
	s_mov_b32 m0, s73
	v_lshl_add_u64 v[182:183], s[56:57], 0, v[166:167]
	global_load_lds_dwordx4 v[180:181], off
	v_lshl_add_u64 v[180:181], v[178:179], 0, s[14:15]
	s_add_i32 m0, s73, 0x2000
	s_nop 0
	global_load_lds_dwordx4 v[180:181], off
	v_lshl_add_u64 v[180:181], s[56:57], 0, v[164:165]
	s_mov_b32 m0, s62
	s_nop 0
	global_load_lds_dwordx4 v[180:181], off
	s_mov_b32 m0, s53
	s_nop 0
	global_load_lds_dwordx4 v[182:183], off
	s_waitcnt vmcnt(8)
	s_waitcnt lgkmcnt(0)
	s_barrier
	v_mfma_scale_f32_16x16x128_f8f6f4 v[94:97], v[26:33], v[192:199], v[94:97], v189, v190 op_sel_hi:[0,0,0]
	v_mfma_scale_f32_16x16x128_f8f6f4 v[86:89], v[18:25], v[192:199], v[86:89], v189, v190 op_sel_hi:[0,0,0]
	v_mfma_scale_f32_16x16x128_f8f6f4 v[78:81], v[26:33], v[200:207], v[78:81], v189, v190 op_sel_hi:[0,0,0]
	v_mfma_scale_f32_16x16x128_f8f6f4 v[70:73], v[18:25], v[200:207], v[70:73], v189, v190 op_sel_hi:[0,0,0]
	v_mfma_scale_f32_16x16x128_f8f6f4 v[62:65], v[26:33], v[208:215], v[62:65], v189, v190 op_sel_hi:[0,0,0]
	v_mfma_scale_f32_16x16x128_f8f6f4 v[54:57], v[18:25], v[208:215], v[54:57], v189, v190 op_sel_hi:[0,0,0]
	v_mfma_scale_f32_16x16x128_f8f6f4 v[46:49], v[26:33], v[220:227], v[46:49], v189, v190 op_sel_hi:[0,0,0]
	v_mfma_scale_f32_16x16x128_f8f6f4 v[38:41], v[18:25], v[220:227], v[38:41], v189, v190 op_sel_hi:[0,0,0]
	v_mfma_scale_f32_16x16x128_f8f6f4 v[90:93], v[10:17], v[192:199], v[90:93], v189, v190 op_sel_hi:[0,0,0]
	v_mfma_scale_f32_16x16x128_f8f6f4 v[82:85], v[2:9], v[192:199], v[82:85], v189, v190 op_sel_hi:[0,0,0]
	v_mfma_scale_f32_16x16x128_f8f6f4 v[74:77], v[10:17], v[200:207], v[74:77], v189, v190 op_sel_hi:[0,0,0]
	v_mfma_scale_f32_16x16x128_f8f6f4 v[66:69], v[2:9], v[200:207], v[66:69], v189, v190 op_sel_hi:[0,0,0]
	v_mfma_scale_f32_16x16x128_f8f6f4 v[58:61], v[10:17], v[208:215], v[58:61], v189, v190 op_sel_hi:[0,0,0]
	v_mfma_scale_f32_16x16x128_f8f6f4 v[50:53], v[2:9], v[208:215], v[50:53], v189, v190 op_sel_hi:[0,0,0]
	v_mfma_scale_f32_16x16x128_f8f6f4 v[42:45], v[10:17], v[220:227], v[42:45], v189, v190 op_sel_hi:[0,0,0]
	v_mfma_scale_f32_16x16x128_f8f6f4 v[34:37], v[2:9], v[220:227], v[34:37], v189, v190 op_sel_hi:[0,0,0]
	s_barrier
	s_add_i32 s73, 0, 0x18000
	s_add_i32 s74, 0, 0x1c000
	v_add_u32_e32 v14, s73, v184
	v_add_u32_e32 v30, s74, v184
	ds_read_b128 v[2:5], v14
	ds_read_b128 v[6:9], v14 offset:1024
	ds_read_b128 v[10:13], v14 offset:2048
	ds_read_b128 v[14:17], v14 offset:3072
	ds_read_b128 v[18:21], v30
	ds_read_b128 v[22:25], v30 offset:1024
	ds_read_b128 v[26:29], v30 offset:2048
	ds_read_b128 v[30:33], v30 offset:3072
	s_add_u32 s56, s56, 0x40000
	s_addc_u32 s57, s57, 0
	s_mov_b32 m0, s63
	v_lshl_add_u64 v[216:217], s[56:57], 0, v[164:165]
	ds_read_b128 v[192:195], v188 offset:32768
	ds_read_b128 v[196:199], v188 offset:33792
	ds_read_b128 v[200:203], v188 offset:34816
	ds_read_b128 v[204:207], v188 offset:35840
	ds_read_b128 v[208:211], v188 offset:36864
	ds_read_b128 v[212:215], v188 offset:37888
	ds_read_b128 v[220:223], v188 offset:38912
	ds_read_b128 v[224:227], v188 offset:39936
	global_load_lds_dwordx4 v[216:217], off
	v_lshl_add_u64 v[216:217], s[56:57], 0, v[166:167]
	s_mov_b32 m0, s64
	s_nop 0
	global_load_lds_dwordx4 v[216:217], off
	s_waitcnt vmcnt(8)
	s_waitcnt lgkmcnt(0)
	s_barrier
	v_mfma_scale_f32_16x16x128_f8f6f4 v[158:161], v[2:9], v[192:199], v[158:161], v189, v190 op_sel_hi:[0,0,0]
	v_mfma_scale_f32_16x16x128_f8f6f4 v[150:153], v[10:17], v[192:199], v[150:153], v189, v190 op_sel_hi:[0,0,0]
	v_mfma_scale_f32_16x16x128_f8f6f4 v[142:145], v[2:9], v[200:207], v[142:145], v189, v190 op_sel_hi:[0,0,0]
	v_mfma_scale_f32_16x16x128_f8f6f4 v[134:137], v[10:17], v[200:207], v[134:137], v189, v190 op_sel_hi:[0,0,0]
	v_mfma_scale_f32_16x16x128_f8f6f4 v[126:129], v[2:9], v[208:215], v[126:129], v189, v190 op_sel_hi:[0,0,0]
	v_mfma_scale_f32_16x16x128_f8f6f4 v[118:121], v[10:17], v[208:215], v[118:121], v189, v190 op_sel_hi:[0,0,0]
	v_mfma_scale_f32_16x16x128_f8f6f4 v[110:113], v[2:9], v[220:227], v[110:113], v189, v190 op_sel_hi:[0,0,0]
	v_mfma_scale_f32_16x16x128_f8f6f4 v[102:105], v[10:17], v[220:227], v[102:105], v189, v190 op_sel_hi:[0,0,0]
	v_mfma_scale_f32_16x16x128_f8f6f4 v[154:157], v[18:25], v[192:199], v[154:157], v189, v190 op_sel_hi:[0,0,0]
	v_mfma_scale_f32_16x16x128_f8f6f4 v[146:149], v[26:33], v[192:199], v[146:149], v189, v190 op_sel_hi:[0,0,0]
	v_mfma_scale_f32_16x16x128_f8f6f4 v[138:141], v[18:25], v[200:207], v[138:141], v189, v190 op_sel_hi:[0,0,0]
	v_mfma_scale_f32_16x16x128_f8f6f4 v[130:133], v[26:33], v[200:207], v[130:133], v189, v190 op_sel_hi:[0,0,0]
	v_mfma_scale_f32_16x16x128_f8f6f4 v[122:125], v[18:25], v[208:215], v[122:125], v189, v190 op_sel_hi:[0,0,0]
	v_mfma_scale_f32_16x16x128_f8f6f4 v[114:117], v[26:33], v[208:215], v[114:117], v189, v190 op_sel_hi:[0,0,0]
	v_mfma_scale_f32_16x16x128_f8f6f4 v[106:109], v[18:25], v[220:227], v[106:109], v189, v190 op_sel_hi:[0,0,0]
	v_mfma_scale_f32_16x16x128_f8f6f4 v[98:101], v[26:33], v[220:227], v[98:101], v189, v190 op_sel_hi:[0,0,0]
	s_barrier
	s_add_i32 s56, s73, s61
	v_lshl_add_u64 v[216:217], v[178:179], 0, s[20:21]
	s_mov_b32 m0, s56
	ds_read_b128 v[192:195], v188 offset:49152
	ds_read_b128 v[196:199], v188 offset:50176
	ds_read_b128 v[200:203], v188 offset:51200
	ds_read_b128 v[204:207], v188 offset:52224
	ds_read_b128 v[208:211], v188 offset:53248
	ds_read_b128 v[212:215], v188 offset:54272
	ds_read_b128 v[220:223], v188 offset:55296
	ds_read_b128 v[224:227], v188 offset:56320
	global_load_lds_dwordx4 v[216:217], off
	v_lshl_add_u64 v[216:217], v[178:179], 0, s[22:23]
	s_add_i32 m0, s56, 0x2000
	s_add_i32 s56, s74, s61
	global_load_lds_dwordx4 v[216:217], off
	v_lshl_add_u64 v[216:217], v[178:179], 0, s[26:27]
	s_mov_b32 m0, s56
	v_lshl_add_u64 v[178:179], v[178:179], 0, s[36:37]
	global_load_lds_dwordx4 v[216:217], off
	s_add_i32 m0, s56, 0x2000
	s_nop 0
	global_load_lds_dwordx4 v[178:179], off
	v_lshl_add_u64 v[178:179], v[180:181], 0, s[24:25]
	s_mov_b32 m0, s66
	s_nop 0
	global_load_lds_dwordx4 v[178:179], off
	v_lshl_add_u64 v[178:179], v[182:183], 0, s[24:25]
	s_mov_b32 m0, s67
	s_nop 0
	global_load_lds_dwordx4 v[178:179], off
	s_waitcnt vmcnt(8)
	s_waitcnt lgkmcnt(0)
	s_barrier
	v_mfma_scale_f32_16x16x128_f8f6f4 v[94:97], v[2:9], v[192:199], v[94:97], v189, v190 op_sel_hi:[0,0,0]
	v_mfma_scale_f32_16x16x128_f8f6f4 v[86:89], v[10:17], v[192:199], v[86:89], v189, v190 op_sel_hi:[0,0,0]
	v_mfma_scale_f32_16x16x128_f8f6f4 v[78:81], v[2:9], v[200:207], v[78:81], v189, v190 op_sel_hi:[0,0,0]
	v_mfma_scale_f32_16x16x128_f8f6f4 v[70:73], v[10:17], v[200:207], v[70:73], v189, v190 op_sel_hi:[0,0,0]
	v_mfma_scale_f32_16x16x128_f8f6f4 v[62:65], v[2:9], v[208:215], v[62:65], v189, v190 op_sel_hi:[0,0,0]
	v_mfma_scale_f32_16x16x128_f8f6f4 v[54:57], v[10:17], v[208:215], v[54:57], v189, v190 op_sel_hi:[0,0,0]
	v_mfma_scale_f32_16x16x128_f8f6f4 v[46:49], v[2:9], v[220:227], v[46:49], v189, v190 op_sel_hi:[0,0,0]
	v_mfma_scale_f32_16x16x128_f8f6f4 v[38:41], v[10:17], v[220:227], v[38:41], v189, v190 op_sel_hi:[0,0,0]
	v_mfma_scale_f32_16x16x128_f8f6f4 v[90:93], v[18:25], v[192:199], v[90:93], v189, v190 op_sel_hi:[0,0,0]
	v_mfma_scale_f32_16x16x128_f8f6f4 v[82:85], v[26:33], v[192:199], v[82:85], v189, v190 op_sel_hi:[0,0,0]
	v_mfma_scale_f32_16x16x128_f8f6f4 v[74:77], v[18:25], v[200:207], v[74:77], v189, v190 op_sel_hi:[0,0,0]
	v_mfma_scale_f32_16x16x128_f8f6f4 v[66:69], v[26:33], v[200:207], v[66:69], v189, v190 op_sel_hi:[0,0,0]
	v_mfma_scale_f32_16x16x128_f8f6f4 v[58:61], v[18:25], v[208:215], v[58:61], v189, v190 op_sel_hi:[0,0,0]
	v_mfma_scale_f32_16x16x128_f8f6f4 v[50:53], v[26:33], v[208:215], v[50:53], v189, v190 op_sel_hi:[0,0,0]
	v_mfma_scale_f32_16x16x128_f8f6f4 v[42:45], v[18:25], v[220:227], v[42:45], v189, v190 op_sel_hi:[0,0,0]
	v_mfma_scale_f32_16x16x128_f8f6f4 v[34:37], v[26:33], v[220:227], v[34:37], v189, v190 op_sel_hi:[0,0,0]
	s_barrier
	s_add_i32 s49, s49, 2
	s_add_u32 s4, s4, 0x100
	s_addc_u32 s5, s5, 0
	s_cmp_gt_u32 s49, 13
	v_lshl_add_u64 v[176:177], v[176:177], 0, s[40:41]
	s_cbranch_scc0 .LBB0_1497
	s_and_b64 vcc, exec, s[38:39]
	s_cbranch_vccz .LBB0_1500
	s_barrier

.LBB0_1568:
	ds_read_b128 v[26:29], v186
	ds_read_b128 v[30:33], v186 offset:1024
	ds_read_b128 v[18:21], v186 offset:2048
	ds_read_b128 v[22:25], v186 offset:3072
	ds_read_b128 v[10:13], v187
	ds_read_b128 v[14:17], v187 offset:1024
	ds_read_b128 v[2:5], v187 offset:2048
	ds_read_b128 v[6:9], v187 offset:3072
	s_add_u32 s58, s56, 0xfff50080
	s_addc_u32 s59, s57, -1
	s_cmp_eq_u32 s53, 40
	s_cselect_b64 vcc, -1, 0
	s_cselect_b32 s59, s5, s59
	s_cselect_b32 s58, s4, s58
	v_cndmask_b32_e32 v179, v177, v175, vcc
	v_cndmask_b32_e32 v178, v176, v174, vcc
	v_lshl_add_u64 v[180:181], s[56:57], 0, v[170:171]
	s_add_i32 m0, s61, 0xc000
	ds_read_b128 v[192:195], v188
	ds_read_b128 v[196:199], v188 offset:1024
	ds_read_b128 v[200:203], v188 offset:2048
	ds_read_b128 v[204:207], v188 offset:3072
	ds_read_b128 v[208:211], v188 offset:4096
	ds_read_b128 v[212:215], v188 offset:5120
	ds_read_b128 v[220:223], v188 offset:6144
	ds_read_b128 v[224:227], v188 offset:7168
	global_load_lds_dwordx4 v[180:181], off
	v_lshl_add_u64 v[180:181], s[56:57], 0, v[172:173]
	s_add_i32 m0, s61, 0xe000
	s_nop 0
	global_load_lds_dwordx4 v[180:181], off
	s_waitcnt vmcnt(8)
	s_waitcnt lgkmcnt(0)
	s_barrier
	v_mfma_scale_f32_16x16x128_f8f6f4 v[158:161], v[26:33], v[192:199], v[158:161], v189, v190 op_sel_hi:[0,0,0]
	v_mfma_scale_f32_16x16x128_f8f6f4 v[154:157], v[18:25], v[192:199], v[154:157], v189, v190 op_sel_hi:[0,0,0]
	v_mfma_scale_f32_16x16x128_f8f6f4 v[150:153], v[26:33], v[200:207], v[150:153], v189, v190 op_sel_hi:[0,0,0]
	v_mfma_scale_f32_16x16x128_f8f6f4 v[142:145], v[18:25], v[200:207], v[142:145], v189, v190 op_sel_hi:[0,0,0]
	v_mfma_scale_f32_16x16x128_f8f6f4 v[134:137], v[26:33], v[208:215], v[134:137], v189, v190 op_sel_hi:[0,0,0]
	v_mfma_scale_f32_16x16x128_f8f6f4 v[126:129], v[18:25], v[208:215], v[126:129], v189, v190 op_sel_hi:[0,0,0]
	v_mfma_scale_f32_16x16x128_f8f6f4 v[118:121], v[26:33], v[220:227], v[118:121], v189, v190 op_sel_hi:[0,0,0]
	v_mfma_scale_f32_16x16x128_f8f6f4 v[110:113], v[18:25], v[220:227], v[110:113], v189, v190 op_sel_hi:[0,0,0]
	v_mfma_scale_f32_16x16x128_f8f6f4 v[146:149], v[10:17], v[192:199], v[146:149], v189, v190 op_sel_hi:[0,0,0]
	v_mfma_scale_f32_16x16x128_f8f6f4 v[138:141], v[2:9], v[192:199], v[138:141], v189, v190 op_sel_hi:[0,0,0]
	v_mfma_scale_f32_16x16x128_f8f6f4 v[130:133], v[10:17], v[200:207], v[130:133], v189, v190 op_sel_hi:[0,0,0]
	v_mfma_scale_f32_16x16x128_f8f6f4 v[122:125], v[2:9], v[200:207], v[122:125], v189, v190 op_sel_hi:[0,0,0]
	v_mfma_scale_f32_16x16x128_f8f6f4 v[114:117], v[10:17], v[208:215], v[114:117], v189, v190 op_sel_hi:[0,0,0]
	v_mfma_scale_f32_16x16x128_f8f6f4 v[106:109], v[2:9], v[208:215], v[106:109], v189, v190 op_sel_hi:[0,0,0]
	v_mfma_scale_f32_16x16x128_f8f6f4 v[102:105], v[10:17], v[220:227], v[102:105], v189, v190 op_sel_hi:[0,0,0]
	v_mfma_scale_f32_16x16x128_f8f6f4 v[98:101], v[2:9], v[220:227], v[98:101], v189, v190 op_sel_hi:[0,0,0]
	s_barrier
	s_add_i32 s80, s69, s33
	v_lshl_add_u64 v[178:179], v[178:179], 0, v[164:165]
	s_mov_b32 m0, s80
	ds_read_b128 v[192:195], v188 offset:16384
	ds_read_b128 v[196:199], v188 offset:17408
	ds_read_b128 v[200:203], v188 offset:18432
	ds_read_b128 v[204:207], v188 offset:19456
	ds_read_b128 v[208:211], v188 offset:20480
	ds_read_b128 v[212:215], v188 offset:21504
	ds_read_b128 v[220:223], v188 offset:22528
	ds_read_b128 v[224:227], v188 offset:23552
	global_load_lds_dwordx4 v[178:179], off
	v_lshl_add_u64 v[180:181], v[178:179], 0, s[10:11]
	s_add_i32 m0, s80, 0x2000
	s_add_i32 s80, s70, s33
	global_load_lds_dwordx4 v[180:181], off
	v_lshl_add_u64 v[180:181], v[178:179], 0, s[12:13]
	s_mov_b32 m0, s80
	v_lshl_add_u64 v[182:183], s[58:59], 0, v[168:169]
	global_load_lds_dwordx4 v[180:181], off
	v_lshl_add_u64 v[180:181], v[178:179], 0, s[14:15]
	s_add_i32 m0, s80, 0x2000
	s_nop 0
	global_load_lds_dwordx4 v[180:181], off
	v_lshl_add_u64 v[180:181], s[58:59], 0, v[166:167]
	s_mov_b32 m0, s61
	s_nop 0
	global_load_lds_dwordx4 v[180:181], off
	s_mov_b32 m0, s62
	s_nop 0
	global_load_lds_dwordx4 v[182:183], off
	s_waitcnt vmcnt(8)
	s_waitcnt lgkmcnt(0)
	s_barrier
	v_mfma_scale_f32_16x16x128_f8f6f4 v[94:97], v[26:33], v[192:199], v[94:97], v189, v190 op_sel_hi:[0,0,0]
	v_mfma_scale_f32_16x16x128_f8f6f4 v[90:93], v[18:25], v[192:199], v[90:93], v189, v190 op_sel_hi:[0,0,0]
	v_mfma_scale_f32_16x16x128_f8f6f4 v[86:89], v[26:33], v[200:207], v[86:89], v189, v190 op_sel_hi:[0,0,0]
	v_mfma_scale_f32_16x16x128_f8f6f4 v[78:81], v[18:25], v[200:207], v[78:81], v189, v190 op_sel_hi:[0,0,0]
	v_mfma_scale_f32_16x16x128_f8f6f4 v[70:73], v[26:33], v[208:215], v[70:73], v189, v190 op_sel_hi:[0,0,0]
	v_mfma_scale_f32_16x16x128_f8f6f4 v[62:65], v[18:25], v[208:215], v[62:65], v189, v190 op_sel_hi:[0,0,0]
	v_mfma_scale_f32_16x16x128_f8f6f4 v[54:57], v[26:33], v[220:227], v[54:57], v189, v190 op_sel_hi:[0,0,0]
	v_mfma_scale_f32_16x16x128_f8f6f4 v[46:49], v[18:25], v[220:227], v[46:49], v189, v190 op_sel_hi:[0,0,0]
	v_mfma_scale_f32_16x16x128_f8f6f4 v[82:85], v[10:17], v[192:199], v[82:85], v189, v190 op_sel_hi:[0,0,0]
	v_mfma_scale_f32_16x16x128_f8f6f4 v[74:77], v[2:9], v[192:199], v[74:77], v189, v190 op_sel_hi:[0,0,0]
	v_mfma_scale_f32_16x16x128_f8f6f4 v[66:69], v[10:17], v[200:207], v[66:69], v189, v190 op_sel_hi:[0,0,0]
	v_mfma_scale_f32_16x16x128_f8f6f4 v[58:61], v[2:9], v[200:207], v[58:61], v189, v190 op_sel_hi:[0,0,0]
	v_mfma_scale_f32_16x16x128_f8f6f4 v[50:53], v[10:17], v[208:215], v[50:53], v189, v190 op_sel_hi:[0,0,0]
	v_mfma_scale_f32_16x16x128_f8f6f4 v[42:45], v[2:9], v[208:215], v[42:45], v189, v190 op_sel_hi:[0,0,0]
	v_mfma_scale_f32_16x16x128_f8f6f4 v[38:41], v[10:17], v[220:227], v[38:41], v189, v190 op_sel_hi:[0,0,0]
	v_mfma_scale_f32_16x16x128_f8f6f4 v[34:37], v[2:9], v[220:227], v[34:37], v189, v190 op_sel_hi:[0,0,0]
	s_barrier
	s_add_i32 s80, 0, 0x18000
	s_add_i32 s81, 0, 0x1c000
	v_add_u32_e32 v14, s80, v184
	v_add_u32_e32 v30, s81, v184
	ds_read_b128 v[2:5], v14
	ds_read_b128 v[6:9], v14 offset:1024
	ds_read_b128 v[10:13], v14 offset:2048
	ds_read_b128 v[14:17], v14 offset:3072
	ds_read_b128 v[18:21], v30
	ds_read_b128 v[22:25], v30 offset:1024
	ds_read_b128 v[26:29], v30 offset:2048
	ds_read_b128 v[30:33], v30 offset:3072
	s_add_u32 s58, s58, 0xb0000
	s_addc_u32 s59, s59, 0
	s_mov_b32 m0, s63
	v_lshl_add_u64 v[216:217], s[58:59], 0, v[166:167]
	ds_read_b128 v[192:195], v188 offset:32768
	ds_read_b128 v[196:199], v188 offset:33792
	ds_read_b128 v[200:203], v188 offset:34816
	ds_read_b128 v[204:207], v188 offset:35840
	ds_read_b128 v[208:211], v188 offset:36864
	ds_read_b128 v[212:215], v188 offset:37888
	ds_read_b128 v[220:223], v188 offset:38912
	ds_read_b128 v[224:227], v188 offset:39936
	global_load_lds_dwordx4 v[216:217], off
	v_lshl_add_u64 v[216:217], s[58:59], 0, v[168:169]
	s_mov_b32 m0, s64
	s_nop 0
	global_load_lds_dwordx4 v[216:217], off
	s_waitcnt vmcnt(8)
	s_waitcnt lgkmcnt(0)
	s_barrier
	v_mfma_scale_f32_16x16x128_f8f6f4 v[158:161], v[2:9], v[192:199], v[158:161], v189, v190 op_sel_hi:[0,0,0]
	v_mfma_scale_f32_16x16x128_f8f6f4 v[154:157], v[10:17], v[192:199], v[154:157], v189, v190 op_sel_hi:[0,0,0]
	v_mfma_scale_f32_16x16x128_f8f6f4 v[150:153], v[2:9], v[200:207], v[150:153], v189, v190 op_sel_hi:[0,0,0]
	v_mfma_scale_f32_16x16x128_f8f6f4 v[142:145], v[10:17], v[200:207], v[142:145], v189, v190 op_sel_hi:[0,0,0]
	v_mfma_scale_f32_16x16x128_f8f6f4 v[134:137], v[2:9], v[208:215], v[134:137], v189, v190 op_sel_hi:[0,0,0]
	v_mfma_scale_f32_16x16x128_f8f6f4 v[126:129], v[10:17], v[208:215], v[126:129], v189, v190 op_sel_hi:[0,0,0]
	v_mfma_scale_f32_16x16x128_f8f6f4 v[118:121], v[2:9], v[220:227], v[118:121], v189, v190 op_sel_hi:[0,0,0]
	v_mfma_scale_f32_16x16x128_f8f6f4 v[110:113], v[10:17], v[220:227], v[110:113], v189, v190 op_sel_hi:[0,0,0]
	v_mfma_scale_f32_16x16x128_f8f6f4 v[146:149], v[18:25], v[192:199], v[146:149], v189, v190 op_sel_hi:[0,0,0]
	v_mfma_scale_f32_16x16x128_f8f6f4 v[138:141], v[26:33], v[192:199], v[138:141], v189, v190 op_sel_hi:[0,0,0]
	v_mfma_scale_f32_16x16x128_f8f6f4 v[130:133], v[18:25], v[200:207], v[130:133], v189, v190 op_sel_hi:[0,0,0]
	v_mfma_scale_f32_16x16x128_f8f6f4 v[122:125], v[26:33], v[200:207], v[122:125], v189, v190 op_sel_hi:[0,0,0]
	v_mfma_scale_f32_16x16x128_f8f6f4 v[114:117], v[18:25], v[208:215], v[114:117], v189, v190 op_sel_hi:[0,0,0]
	v_mfma_scale_f32_16x16x128_f8f6f4 v[106:109], v[26:33], v[208:215], v[106:109], v189, v190 op_sel_hi:[0,0,0]
	v_mfma_scale_f32_16x16x128_f8f6f4 v[102:105], v[18:25], v[220:227], v[102:105], v189, v190 op_sel_hi:[0,0,0]
	v_mfma_scale_f32_16x16x128_f8f6f4 v[98:101], v[26:33], v[220:227], v[98:101], v189, v190 op_sel_hi:[0,0,0]
	s_barrier
	s_add_i32 s58, s80, s33
	v_lshl_add_u64 v[216:217], v[178:179], 0, s[24:25]
	s_mov_b32 m0, s58
	ds_read_b128 v[192:195], v188 offset:49152
	ds_read_b128 v[196:199], v188 offset:50176
	ds_read_b128 v[200:203], v188 offset:51200
	ds_read_b128 v[204:207], v188 offset:52224
	ds_read_b128 v[208:211], v188 offset:53248
	ds_read_b128 v[212:215], v188 offset:54272
	ds_read_b128 v[220:223], v188 offset:55296
	ds_read_b128 v[224:227], v188 offset:56320
	global_load_lds_dwordx4 v[216:217], off
	v_lshl_add_u64 v[216:217], v[178:179], 0, s[26:27]
	s_add_i32 m0, s58, 0x2000
	s_add_i32 s58, s81, s33
	global_load_lds_dwordx4 v[216:217], off
	v_lshl_add_u64 v[216:217], v[178:179], 0, s[38:39]
	s_mov_b32 m0, s58
	v_lshl_add_u64 v[178:179], v[178:179], 0, s[40:41]
	global_load_lds_dwordx4 v[216:217], off
	s_add_i32 m0, s58, 0x2000
	s_nop 0
	global_load_lds_dwordx4 v[178:179], off
	v_lshl_add_u64 v[178:179], v[180:181], 0, s[36:37]
	s_mov_b32 m0, s66
	s_nop 0
	global_load_lds_dwordx4 v[178:179], off
	v_lshl_add_u64 v[178:179], v[182:183], 0, s[36:37]
	s_mov_b32 m0, s67
	s_nop 0
	global_load_lds_dwordx4 v[178:179], off
	s_waitcnt vmcnt(8)
	s_waitcnt lgkmcnt(0)
	s_barrier
	v_mfma_scale_f32_16x16x128_f8f6f4 v[94:97], v[2:9], v[192:199], v[94:97], v189, v190 op_sel_hi:[0,0,0]
	v_mfma_scale_f32_16x16x128_f8f6f4 v[90:93], v[10:17], v[192:199], v[90:93], v189, v190 op_sel_hi:[0,0,0]
	v_mfma_scale_f32_16x16x128_f8f6f4 v[86:89], v[2:9], v[200:207], v[86:89], v189, v190 op_sel_hi:[0,0,0]
	v_mfma_scale_f32_16x16x128_f8f6f4 v[78:81], v[10:17], v[200:207], v[78:81], v189, v190 op_sel_hi:[0,0,0]
	v_mfma_scale_f32_16x16x128_f8f6f4 v[70:73], v[2:9], v[208:215], v[70:73], v189, v190 op_sel_hi:[0,0,0]
	v_mfma_scale_f32_16x16x128_f8f6f4 v[62:65], v[10:17], v[208:215], v[62:65], v189, v190 op_sel_hi:[0,0,0]
	v_mfma_scale_f32_16x16x128_f8f6f4 v[54:57], v[2:9], v[220:227], v[54:57], v189, v190 op_sel_hi:[0,0,0]
	v_mfma_scale_f32_16x16x128_f8f6f4 v[46:49], v[10:17], v[220:227], v[46:49], v189, v190 op_sel_hi:[0,0,0]
	v_mfma_scale_f32_16x16x128_f8f6f4 v[82:85], v[18:25], v[192:199], v[82:85], v189, v190 op_sel_hi:[0,0,0]
	v_mfma_scale_f32_16x16x128_f8f6f4 v[74:77], v[26:33], v[192:199], v[74:77], v189, v190 op_sel_hi:[0,0,0]
	v_mfma_scale_f32_16x16x128_f8f6f4 v[66:69], v[18:25], v[200:207], v[66:69], v189, v190 op_sel_hi:[0,0,0]
	v_mfma_scale_f32_16x16x128_f8f6f4 v[58:61], v[26:33], v[200:207], v[58:61], v189, v190 op_sel_hi:[0,0,0]
	v_mfma_scale_f32_16x16x128_f8f6f4 v[50:53], v[18:25], v[208:215], v[50:53], v189, v190 op_sel_hi:[0,0,0]
	v_mfma_scale_f32_16x16x128_f8f6f4 v[42:45], v[26:33], v[208:215], v[42:45], v189, v190 op_sel_hi:[0,0,0]
	v_mfma_scale_f32_16x16x128_f8f6f4 v[38:41], v[18:25], v[220:227], v[38:41], v189, v190 op_sel_hi:[0,0,0]
	v_mfma_scale_f32_16x16x128_f8f6f4 v[34:37], v[26:33], v[220:227], v[34:37], v189, v190 op_sel_hi:[0,0,0]
	s_barrier
	s_add_i32 s53, s53, 2
	s_add_u32 s56, s56, 0x100
	s_addc_u32 s57, s57, 0
	s_cmp_gt_u32 s53, 41
	v_lshl_add_u64 v[176:177], v[176:177], 0, s[44:45]
	s_cbranch_scc0 .LBB0_1568
	s_and_b64 vcc, exec, s[42:43]
	s_cbranch_vccz .LBB0_1571
	s_barrier
